# v35 + prologue param waits relaxed to vmcnt(14) so row group 1 loads issue before group 0 lands
# baseline (speedup 1.0000x reference)
.LBB1_4:
	s_or_b64 exec, exec, s[4:5]
	s_load_dwordx2 s[30:31], s[0:1], 0x68
	s_load_dwordx8 s[12:19], s[0:1], 0x48
	v_lshlrev_b32_e32 v13, 1, v0
	s_and_saveexec_b64 s[4:5], vcc
	s_cbranch_execz .LBB1_6
	s_waitcnt vmcnt(14)
	v_cvt_f16_f32_e32 v5, v5
	v_mov_b32_e32 v6, 0x19860
	v_add_u32_e32 v7, 0x19060, v2
	v_add_u32_e32 v2, 0x19460, v2
	v_lshl_add_u32 v6, v0, 1, v6
	ds_write_b32 v2, v3
	ds_write_b32 v7, v4
	ds_write_b16 v6, v5
.LBB1_6:
	s_or_b64 exec, exec, s[4:5]
	v_mov_b32_e32 v6, 0x18010
	v_mov_b32_e32 v2, 0x18000
	s_waitcnt lgkmcnt(0)
	s_barrier
	s_waitcnt vmcnt(14)
	ds_read_b128 v[2:5], v2
	ds_read_b128 v[6:9], v6
	s_load_dwordx4 s[36:39], s[0:1], 0x20
	s_movk_i32 s0, 0x2000
	v_lshrrev_b32_e32 v125, 4, v131
	s_waitcnt lgkmcnt(0)
	v_mov_b32_e32 v14, v2
	v_mov_b32_e32 v15, v6
	v_mov_b32_e32 v6, v3
	v_pk_add_f32 v[2:3], v[14:15], v[6:7]
	v_mov_b32_e32 v6, v4
	v_mov_b32_e32 v7, v8
	v_mov_b32_e32 v8, v5
	v_pk_add_f32 v[4:5], v[6:7], v[8:9]
	v_mov_b32_e32 v14, 0x18060
	v_pk_add_f32 v[2:3], v[2:3], v[4:5]
	v_add_co_u32_e32 v42, vcc, s0, v82
	v_add_f32_e32 v2, v2, v3
	v_mul_f32_e32 v132, 0x3a800000, v2
	v_and_b32_e32 v107, 15, v0
	v_mov_b32_e32 v2, 0x18020
	v_mov_b32_e32 v3, 0x18030
	v_lshl_add_u32 v13, v13, 2, v14
	v_pk_add_f32 v[10:11], v[10:11], v[132:133] op_sel_hi:[1,0] neg_lo:[0,1] neg_hi:[0,1]
	v_lshlrev_b32_e32 v85, 13, v1
	v_xor_b32_e32 v114, v125, v0
	v_addc_co_u32_e32 v43, vcc, 0, v83, vcc
	s_movk_i32 s0, 0x3000
	ds_read_b128 v[6:9], v2
	ds_read_b128 v[2:5], v3
	ds_write_b64 v13, v[10:11]
	v_lshl_or_b32 v84, v107, 9, v85
	v_lshlrev_b32_e32 v10, 4, v114
	s_movk_i32 s41, 0xf0
	v_add_co_u32_e32 v44, vcc, s0, v82
	v_lshlrev_b32_e32 v130, 2, v12
	v_and_or_b32 v115, v10, s41, v84
	v_addc_co_u32_e32 v45, vcc, 0, v83, vcc
	global_load_dwordx4 v[34:37], v[42:43], off offset:1024 nt
	global_load_dwordx4 v[30:33], v[42:43], off offset:2048 nt
	global_load_dwordx4 v[26:29], v[42:43], off offset:3072 nt
	global_load_dwordx4 v[38:41], v[44:45], off offset:-4096 nt
	global_load_dwordx4 v[22:25], v[44:45], off nt
	global_load_dwordx4 v[18:21], v[44:45], off offset:1024 nt
	global_load_dwordx4 v[14:17], v[44:45], off offset:2048 nt
	global_load_dwordx4 v[10:13], v[44:45], off offset:3072 nt
	s_waitcnt vmcnt(15)
	v_add_f32_e32 v42, v78, v79
	v_add_f32_e32 v43, v80, v81
	v_add_f32_e32 v42, v42, v43
	s_waitcnt vmcnt(14)
	v_add_f32_e32 v43, v74, v75
	v_add_f32_e32 v44, v76, v77
	v_add_f32_e32 v43, v43, v44
	s_waitcnt vmcnt(13)
	v_add_f32_e32 v44, v70, v71
	v_add_f32_e32 v45, v72, v73
	v_add_f32_e32 v44, v44, v45
	s_waitcnt vmcnt(12)
	v_add_f32_e32 v45, v66, v67
	v_add_f32_e32 v49, v68, v69
	v_add_f32_e32 v45, v45, v49
	s_waitcnt vmcnt(11)
	v_add_f32_e32 v49, v62, v63
	v_add_f32_e32 v86, v64, v65
	v_and_b32_e32 v46, 1, v0
	v_add_f32_e32 v49, v49, v86
	s_waitcnt vmcnt(10)
	v_add_f32_e32 v86, v58, v59
	v_add_f32_e32 v88, v60, v61
	v_add_f32_e32 v86, v86, v88
	s_waitcnt vmcnt(9)
	v_add_f32_e32 v88, v54, v55
	v_add_f32_e32 v89, v56, v57
	v_cmp_eq_u32_e64 s[4:5], 1, v46
	v_add_f32_e32 v88, v88, v89
	s_waitcnt vmcnt(8)
	v_add_f32_e32 v89, v50, v51
	v_add_f32_e32 v90, v52, v53
	v_cndmask_b32_e64 v46, v43, v42, s[4:5]
	v_cndmask_b32_e64 v42, v42, v43, s[4:5]
	v_cndmask_b32_e64 v43, v45, v44, s[4:5]
	v_cndmask_b32_e64 v44, v44, v45, s[4:5]
	v_add_f32_e32 v89, v89, v90
	v_cndmask_b32_e64 v45, v49, v86, s[4:5]
	v_add_f32_dpp v43, v43, v44 quad_perm:[1,0,3,2] row_mask:0xf bank_mask:0xf bound_ctrl:1
	v_cndmask_b32_e64 v44, v86, v49, s[4:5]
	v_and_b32_e32 v47, 2, v0
	v_add_f32_dpp v42, v46, v42 quad_perm:[1,0,3,2] row_mask:0xf bank_mask:0xf bound_ctrl:1
	v_add_f32_dpp v44, v44, v45 quad_perm:[1,0,3,2] row_mask:0xf bank_mask:0xf bound_ctrl:1
	v_cndmask_b32_e64 v45, v89, v88, s[4:5]
	v_cndmask_b32_e64 v46, v88, v89, s[4:5]
	v_cmp_eq_u16_e64 s[6:7], 0, v47
	v_and_b32_e32 v48, 4, v0
	v_add_f32_dpp v45, v45, v46 quad_perm:[1,0,3,2] row_mask:0xf bank_mask:0xf bound_ctrl:1
	v_cndmask_b32_e64 v46, v42, v43, s[6:7]
	v_cndmask_b32_e64 v42, v43, v42, s[6:7]
	v_cndmask_b32_e64 v43, v44, v45, s[6:7]
	v_cndmask_b32_e64 v44, v45, v44, s[6:7]
	v_add_f32_dpp v42, v46, v42 quad_perm:[2,3,0,1] row_mask:0xf bank_mask:0xf bound_ctrl:1
	v_cmp_eq_u16_e64 s[8:9], 0, v48
	v_add_f32_dpp v43, v43, v44 quad_perm:[2,3,0,1] row_mask:0xf bank_mask:0xf bound_ctrl:1
	v_lshlrev_b32_e32 v86, 3, v131
	v_cndmask_b32_e64 v44, v42, v43, s[8:9]
	v_cndmask_b32_e64 v42, v43, v42, s[8:9]
	v_mov_b32_e32 v43, v44
	v_and_b32_e32 v87, 8, v87
	v_mov_b32_e32 v116, 0x3727c5ac
	v_mov_b32_dpp v43, v43 row_shl:4 row_mask:0xf bank_mask:0x5
	v_mov_b32_e32 v117, 0x260
	v_bitop3_b32 v141, v125, v0, 4 bitop3:0x36
	v_mov_b32_dpp v43, v44 row_shr:4 row_mask:0xf bank_mask:0xa
	v_add_f32_e32 v42, v42, v43
	v_bitop3_b32 v142, v125, v0, 8 bitop3:0x36
	v_bitop3_b32 v143, v125, v0, 12 bitop3:0x36
	v_add_f32_dpp v42, v42, v42 row_ror:8 row_mask:0xf bank_mask:0xf bound_ctrl:1
	v_mov_b32_e32 v43, v42
	s_nop 1
	v_permlane16_swap_b32_e32 v42, v43
	v_add_f32_e32 v42, v42, v43
	v_mov_b32_e32 v43, v42
	s_nop 1
	v_permlane32_swap_b32_e32 v42, v43
	v_add_f32_e32 v42, v42, v43
	v_mul_f32_e32 v42, 0x3b800000, v42
	s_mov_b32 s3, 0
	v_readlane_b32 s40, v42, 0
	v_readlane_b32 s42, v42, 1
	v_readlane_b32 s44, v42, 2
	v_readlane_b32 s46, v42, 3
	v_readlane_b32 s48, v42, 4
	v_readlane_b32 s50, v42, 5
	v_readlane_b32 s34, v42, 6
	v_readlane_b32 s0, v42, 7
	v_pk_add_f32 v[90:91], v[78:79], s[40:41] op_sel_hi:[1,0] neg_lo:[0,1] neg_hi:[0,1]
	v_pk_add_f32 v[80:81], v[80:81], s[40:41] op_sel_hi:[1,0] neg_lo:[0,1] neg_hi:[0,1]
	v_and_b32_e32 v78, 0x1f0, v86
	v_pk_add_f32 v[76:77], v[76:77], s[42:43] op_sel_hi:[1,0] neg_lo:[0,1] neg_hi:[0,1]
	v_mul_f32_e32 v88, v81, v81
	v_or3_b32 v140, v85, v78, v87
	v_pk_add_f32 v[78:79], v[74:75], s[42:43] op_sel_hi:[1,0] neg_lo:[0,1] neg_hi:[0,1]
	v_mul_f32_e32 v74, v77, v77
	v_fmac_f32_e32 v88, v80, v80
	v_fmac_f32_e32 v74, v76, v76
	v_fmac_f32_e32 v88, v91, v91
	v_fmac_f32_e32 v74, v79, v79
	v_fmac_f32_e32 v88, v90, v90
	v_fmac_f32_e32 v74, v78, v78
	v_cndmask_b32_e64 v75, v74, v88, s[4:5]
	v_cndmask_b32_e64 v74, v88, v74, s[4:5]
	v_mov_b32_e32 v88, 0x1f0
	v_pk_add_f32 v[72:73], v[72:73], s[44:45] op_sel_hi:[1,0] neg_lo:[0,1] neg_hi:[0,1]
	v_add_f32_dpp v89, v75, v74 quad_perm:[1,0,3,2] row_mask:0xf bank_mask:0xf bound_ctrl:1
	v_bitop3_b32 v74, v86, 16, v88 bitop3:0x6c
	v_or3_b32 v138, v85, v74, v87
	v_pk_add_f32 v[74:75], v[70:71], s[44:45] op_sel_hi:[1,0] neg_lo:[0,1] neg_hi:[0,1]
	v_bitop3_b32 v70, v86, 32, v88 bitop3:0x6c
	v_pk_add_f32 v[68:69], v[68:69], s[46:47] op_sel_hi:[1,0] neg_lo:[0,1] neg_hi:[0,1]
	v_mul_f32_e32 v92, v73, v73
	v_or3_b32 v135, v85, v70, v87
	v_pk_add_f32 v[70:71], v[66:67], s[46:47] op_sel_hi:[1,0] neg_lo:[0,1] neg_hi:[0,1]
	v_mul_f32_e32 v66, v69, v69
	v_fmac_f32_e32 v92, v72, v72
	v_fmac_f32_e32 v66, v68, v68
	v_fmac_f32_e32 v92, v75, v75
	v_fmac_f32_e32 v66, v71, v71
	v_fmac_f32_e32 v92, v74, v74
	v_fmac_f32_e32 v66, v70, v70
	v_cndmask_b32_e64 v67, v66, v92, s[4:5]
	v_cndmask_b32_e64 v66, v92, v66, s[4:5]
	v_pk_add_f32 v[64:65], v[64:65], s[48:49] op_sel_hi:[1,0] neg_lo:[0,1] neg_hi:[0,1]
	v_pk_add_f32 v[60:61], v[60:61], s[50:51] op_sel_hi:[1,0] neg_lo:[0,1] neg_hi:[0,1]
	v_add_f32_dpp v66, v67, v66 quad_perm:[1,0,3,2] row_mask:0xf bank_mask:0xf bound_ctrl:1
	v_cndmask_b32_e64 v67, v89, v66, s[6:7]
	v_cndmask_b32_e64 v66, v66, v89, s[6:7]
	v_mul_f32_e32 v92, v65, v65
	v_fmac_f32_e32 v92, v64, v64
	v_add_f32_dpp v89, v67, v66 quad_perm:[2,3,0,1] row_mask:0xf bank_mask:0xf bound_ctrl:1
	v_bitop3_b32 v66, v86, 48, v88 bitop3:0x6c
	v_or3_b32 v134, v85, v66, v87
	v_pk_add_f32 v[66:67], v[62:63], s[48:49] op_sel_hi:[1,0] neg_lo:[0,1] neg_hi:[0,1]
	v_bitop3_b32 v62, v86, 64, v88 bitop3:0x6c
	v_or3_b32 v120, v85, v62, v87
	v_pk_add_f32 v[62:63], v[58:59], s[50:51] op_sel_hi:[1,0] neg_lo:[0,1] neg_hi:[0,1]
	v_mul_f32_e32 v58, v61, v61
	v_fmac_f32_e32 v58, v60, v60
	v_fmac_f32_e32 v92, v67, v67
	v_fmac_f32_e32 v58, v63, v63
	v_fmac_f32_e32 v92, v66, v66
	v_fmac_f32_e32 v58, v62, v62
	v_cndmask_b32_e64 v59, v58, v92, s[4:5]
	v_cndmask_b32_e64 v58, v92, v58, s[4:5]
	v_pk_add_f32 v[56:57], v[56:57], s[34:35] op_sel_hi:[1,0] neg_lo:[0,1] neg_hi:[0,1]
	s_mov_b32 s25, 0x3e6d3387
	v_add_f32_dpp v92, v59, v58 quad_perm:[1,0,3,2] row_mask:0xf bank_mask:0xf bound_ctrl:1
	v_pk_add_f32 v[58:59], v[54:55], s[34:35] op_sel_hi:[1,0] neg_lo:[0,1] neg_hi:[0,1]
	v_pk_add_f32 v[54:55], v[50:51], s[0:1] op_sel_hi:[1,0] neg_lo:[0,1] neg_hi:[0,1]
	v_pk_add_f32 v[50:51], v[52:53], s[0:1] op_sel_hi:[1,0] neg_lo:[0,1] neg_hi:[0,1]
	v_mul_f32_e32 v93, v57, v57
	v_mul_f32_e32 v52, v51, v51
	v_fmac_f32_e32 v93, v56, v56
	v_fmac_f32_e32 v52, v50, v50
	v_fmac_f32_e32 v93, v59, v59
	v_fmac_f32_e32 v52, v55, v55
	v_fmac_f32_e32 v93, v58, v58
	v_fmac_f32_e32 v52, v54, v54
	v_cndmask_b32_e64 v53, v52, v93, s[4:5]
	v_cndmask_b32_e64 v52, v93, v52, s[4:5]
	s_mov_b32 s35, 0xf800000
	s_movk_i32 s0, 0x50
	v_add_f32_dpp v52, v53, v52 quad_perm:[1,0,3,2] row_mask:0xf bank_mask:0xf bound_ctrl:1
	v_cndmask_b32_e64 v53, v92, v52, s[6:7]
	v_cndmask_b32_e64 v52, v52, v92, s[6:7]
	s_mov_b32 s24, 0xbf3a00e3
	s_mov_b32 s22, 0x3f07dc22
	v_add_f32_dpp v52, v53, v52 quad_perm:[2,3,0,1] row_mask:0xf bank_mask:0xf bound_ctrl:1
	v_cndmask_b32_e64 v53, v89, v52, s[8:9]
	v_cndmask_b32_e64 v52, v52, v89, s[8:9]
	v_mov_b32_e32 v89, v53
	s_mov_b32 s34, 0xbe11a98e
	s_mov_b32 s40, 0x3e027906
	v_mov_b32_dpp v89, v89 row_shl:4 row_mask:0xf bank_mask:0x5
	s_mov_b32 s33, 5
	s_nop 0
	v_mov_b32_dpp v89, v53 row_shr:4 row_mask:0xf bank_mask:0xa
	v_add_f32_e32 v52, v52, v89
	v_bitop3_b32 v89, v86, s0, v88 bitop3:0x6c
	v_or3_b32 v121, v85, v89, v87
	v_add_f32_dpp v52, v52, v52 row_ror:8 row_mask:0xf bank_mask:0xf bound_ctrl:1
	v_mov_b32_e32 v53, v52
	s_nop 1
	v_permlane16_swap_b32_e32 v52, v53
	v_add_f32_e32 v52, v52, v53
	v_mov_b32_e32 v53, v52
	s_nop 1
	v_permlane32_swap_b32_e32 v52, v53
	v_add_f32_e32 v52, v52, v53
	v_fmamk_f32 v52, v52, 0x3b800000, v116
	v_mul_f32_e32 v53, 0x4f800000, v52
	v_cmp_gt_f32_e32 vcc, s35, v52
	s_nop 1
	v_cndmask_b32_e32 v52, v52, v53, vcc
	v_sqrt_f32_e32 v53, v52
	s_nop 0
	v_add_u32_e32 v89, -1, v53
	v_fma_f32 v92, -v89, v53, v52
	v_cmp_ge_f32_e64 s[0:1], 0, v92
	v_add_u32_e32 v92, 1, v53
	s_nop 0
	v_cndmask_b32_e64 v89, v53, v89, s[0:1]
	v_fma_f32 v53, -v92, v53, v52
	v_cmp_lt_f32_e64 s[0:1], 0, v53
	s_nop 1
	v_cndmask_b32_e64 v53, v89, v92, s[0:1]
	v_mul_f32_e32 v89, 0x37800000, v53
	v_cndmask_b32_e32 v53, v53, v89, vcc
	v_cmp_class_f32_e32 vcc, v52, v117
	s_nop 1
	v_cndmask_b32_e32 v52, v53, v52, vcc
	v_div_scale_f32 v53, s[0:1], v52, v52, 1.0
	v_rcp_f32_e32 v89, v53
	s_movk_i32 s0, 0x60
	v_bitop3_b32 v92, v86, s0, v88 bitop3:0x6c
	v_or3_b32 v118, v85, v92, v87
	v_fma_f32 v92, -v53, v89, 1.0
	v_fmac_f32_e32 v89, v92, v89
	v_div_scale_f32 v92, vcc, 1.0, v52, 1.0
	v_mul_f32_e32 v93, v92, v89
	v_fma_f32 v94, -v53, v93, v92
	v_fmac_f32_e32 v93, v94, v89
	v_fma_f32 v53, -v53, v93, v92
	v_div_fmas_f32 v53, v53, v89, v93
	v_div_fixup_f32 v52, v53, v52, 1.0
	s_waitcnt vmcnt(4)
	v_add_f32_e32 v89, v38, v39
	v_readlane_b32 s0, v52, 0
	s_nop 1
	v_pk_mul_f32 v[90:91], s[0:1], v[90:91] op_sel_hi:[0,1]
	v_pk_fma_f32 v[92:93], v[90:91], v[238:239], v[242:243]
	v_mov_b64_e32 v[90:91], s[24:25]
	v_fma_f32 v53, |v92|, s25, 1.0
	v_pk_mul_f32 v[98:99], v[92:93], v[92:93]
	v_rcp_f32_e32 v96, v53
	v_mul_f32_e32 v53, 0xbf38aa3b, v98
	v_exp_f32_e32 v98, v53
	v_fma_f32 v53, |v93|, s25, 1.0
	v_rcp_f32_e32 v97, v53
	s_mov_b32 s24, 0x3f35f0e3
	v_pk_mul_f32 v[80:81], s[0:1], v[80:81] op_sel_hi:[0,1]
	v_mul_f32_e32 v53, 0xbf38aa3b, v99
	v_pk_fma_f32 v[100:101], v[96:97], s[22:23], v[90:91] op_sel_hi:[1,0,0]
	v_pk_fma_f32 v[80:81], v[80:81], v[240:241], v[244:245]
	v_pk_fma_f32 v[100:101], v[96:97], v[100:101], s[24:25] op_sel_hi:[1,1,0]
	v_and_b32_e32 v95, 0x7fffffff, v93
	v_pk_fma_f32 v[100:101], v[96:97], v[100:101], s[34:35] op_sel_hi:[1,1,0]
	v_and_b32_e32 v94, 0x7fffffff, v92
	v_pk_fma_f32 v[100:101], v[96:97], v[100:101], s[40:41] op_sel_hi:[1,1,0]
	v_exp_f32_e32 v99, v53
	v_pk_mul_f32 v[96:97], v[96:97], v[100:101]
	v_fma_f32 v53, |v80|, s25, 1.0
	v_pk_mul_f32 v[94:95], v[94:95], v[96:97]
	v_rcp_f32_e32 v96, v53
	v_fma_f32 v53, |v81|, s25, 1.0
	v_rcp_f32_e32 v97, v53
	v_max_f32_e32 v92, 0, v92
	v_max_f32_e32 v93, 0, v93
	v_pk_fma_f32 v[92:93], v[98:99], v[94:95], v[92:93] neg_lo:[1,0,0] neg_hi:[1,0,0]
	v_pk_mul_f32 v[98:99], v[80:81], v[80:81]
	v_pk_fma_f32 v[100:101], v[96:97], s[22:23], v[90:91] op_sel_hi:[1,0,0]
	v_mul_f32_e32 v53, 0xbf38aa3b, v98
	v_exp_f32_e32 v98, v53
	v_pk_fma_f32 v[100:101], v[96:97], v[100:101], s[24:25] op_sel_hi:[1,1,0]
	v_mul_f32_e32 v53, 0xbf38aa3b, v99
	v_pk_fma_f32 v[100:101], v[96:97], v[100:101], s[34:35] op_sel_hi:[1,1,0]
	v_exp_f32_e32 v99, v53
	v_pk_fma_f32 v[100:101], v[96:97], v[100:101], s[40:41] op_sel_hi:[1,1,0]
	v_and_b32_e32 v95, 0x7fffffff, v81
	v_and_b32_e32 v94, 0x7fffffff, v80
	v_pk_mul_f32 v[96:97], v[96:97], v[100:101]
	v_readlane_b32 s0, v52, 1
	v_max_f32_e32 v80, 0, v80
	v_max_f32_e32 v81, 0, v81
	v_pk_mul_f32 v[94:95], v[94:95], v[96:97]
	v_pk_mul_f32 v[78:79], s[0:1], v[78:79] op_sel_hi:[0,1]
	v_pk_fma_f32 v[80:81], v[98:99], v[94:95], v[80:81] neg_lo:[1,0,0] neg_hi:[1,0,0]
	v_pk_fma_f32 v[78:79], v[78:79], v[238:239], v[242:243]
	v_cvt_pk_f16_f32 v92, v92, v93
	v_cvt_pk_f16_f32 v93, v80, v81
	v_fma_f32 v53, |v78|, s25, 1.0
	ds_write_b64 v140, v[92:93] offset:32768
	v_rcp_f32_e32 v92, v53
	v_fma_f32 v53, |v79|, s25, 1.0
	v_rcp_f32_e32 v93, v53
	v_pk_mul_f32 v[94:95], v[78:79], v[78:79]
	v_pk_mul_f32 v[76:77], s[0:1], v[76:77] op_sel_hi:[0,1]
	v_mul_f32_e32 v53, 0xbf38aa3b, v94
	v_pk_fma_f32 v[96:97], v[92:93], s[22:23], v[90:91] op_sel_hi:[1,0,0]
	v_exp_f32_e32 v94, v53
	v_pk_fma_f32 v[96:97], v[92:93], v[96:97], s[24:25] op_sel_hi:[1,1,0]
	v_mul_f32_e32 v53, 0xbf38aa3b, v95
	v_pk_fma_f32 v[96:97], v[92:93], v[96:97], s[34:35] op_sel_hi:[1,1,0]
	v_pk_fma_f32 v[76:77], v[76:77], v[240:241], v[244:245]
	v_pk_fma_f32 v[96:97], v[92:93], v[96:97], s[40:41] op_sel_hi:[1,1,0]
	v_and_b32_e32 v81, 0x7fffffff, v79
	v_and_b32_e32 v80, 0x7fffffff, v78
	v_exp_f32_e32 v95, v53
	v_pk_mul_f32 v[92:93], v[92:93], v[96:97]
	v_fma_f32 v53, |v76|, s25, 1.0
	v_pk_mul_f32 v[80:81], v[80:81], v[92:93]
	v_rcp_f32_e32 v92, v53
	v_fma_f32 v53, |v77|, s25, 1.0
	v_rcp_f32_e32 v93, v53
	v_max_f32_e32 v78, 0, v78
	v_max_f32_e32 v79, 0, v79
	v_pk_fma_f32 v[78:79], v[94:95], v[80:81], v[78:79] neg_lo:[1,0,0] neg_hi:[1,0,0]
	v_pk_mul_f32 v[94:95], v[76:77], v[76:77]
	v_pk_fma_f32 v[96:97], v[92:93], s[22:23], v[90:91] op_sel_hi:[1,0,0]
	v_mul_f32_e32 v53, 0xbf38aa3b, v94
	v_exp_f32_e32 v94, v53
	v_pk_fma_f32 v[96:97], v[92:93], v[96:97], s[24:25] op_sel_hi:[1,1,0]
	v_mul_f32_e32 v53, 0xbf38aa3b, v95
	v_pk_fma_f32 v[96:97], v[92:93], v[96:97], s[34:35] op_sel_hi:[1,1,0]
	v_exp_f32_e32 v95, v53
	v_pk_fma_f32 v[96:97], v[92:93], v[96:97], s[40:41] op_sel_hi:[1,1,0]
	v_and_b32_e32 v81, 0x7fffffff, v77
	v_and_b32_e32 v80, 0x7fffffff, v76
	v_pk_mul_f32 v[92:93], v[92:93], v[96:97]
	v_readlane_b32 s0, v52, 2
	v_max_f32_e32 v76, 0, v76
	v_max_f32_e32 v77, 0, v77
	v_pk_mul_f32 v[80:81], v[80:81], v[92:93]
	v_pk_mul_f32 v[74:75], s[0:1], v[74:75] op_sel_hi:[0,1]
	v_pk_fma_f32 v[76:77], v[94:95], v[80:81], v[76:77] neg_lo:[1,0,0] neg_hi:[1,0,0]
	v_pk_fma_f32 v[74:75], v[74:75], v[238:239], v[242:243]
	v_cvt_pk_f16_f32 v78, v78, v79
	v_cvt_pk_f16_f32 v79, v76, v77
	v_fma_f32 v53, |v74|, s25, 1.0
	ds_write_b64 v138, v[78:79] offset:33280
	v_rcp_f32_e32 v78, v53
	v_fma_f32 v53, |v75|, s25, 1.0
	v_rcp_f32_e32 v79, v53
	v_pk_mul_f32 v[80:81], v[74:75], v[74:75]
	v_pk_mul_f32 v[72:73], s[0:1], v[72:73] op_sel_hi:[0,1]
	v_mul_f32_e32 v53, 0xbf38aa3b, v80
	v_pk_fma_f32 v[92:93], v[78:79], s[22:23], v[90:91] op_sel_hi:[1,0,0]
	v_exp_f32_e32 v80, v53
	v_pk_fma_f32 v[92:93], v[78:79], v[92:93], s[24:25] op_sel_hi:[1,1,0]
	v_mul_f32_e32 v53, 0xbf38aa3b, v81
	v_pk_fma_f32 v[92:93], v[78:79], v[92:93], s[34:35] op_sel_hi:[1,1,0]
	v_pk_fma_f32 v[72:73], v[72:73], v[240:241], v[244:245]
	v_pk_fma_f32 v[92:93], v[78:79], v[92:93], s[40:41] op_sel_hi:[1,1,0]
	v_and_b32_e32 v77, 0x7fffffff, v75
	v_and_b32_e32 v76, 0x7fffffff, v74
	v_exp_f32_e32 v81, v53
	v_pk_mul_f32 v[78:79], v[78:79], v[92:93]
	v_fma_f32 v53, |v72|, s25, 1.0
	v_pk_mul_f32 v[76:77], v[76:77], v[78:79]
	v_rcp_f32_e32 v78, v53
	v_fma_f32 v53, |v73|, s25, 1.0
	v_rcp_f32_e32 v79, v53
	v_max_f32_e32 v74, 0, v74
	v_max_f32_e32 v75, 0, v75
	v_pk_fma_f32 v[74:75], v[80:81], v[76:77], v[74:75] neg_lo:[1,0,0] neg_hi:[1,0,0]
	v_pk_mul_f32 v[80:81], v[72:73], v[72:73]
	v_pk_fma_f32 v[92:93], v[78:79], s[22:23], v[90:91] op_sel_hi:[1,0,0]
	v_mul_f32_e32 v53, 0xbf38aa3b, v80
	v_exp_f32_e32 v80, v53
	v_pk_fma_f32 v[92:93], v[78:79], v[92:93], s[24:25] op_sel_hi:[1,1,0]
	v_mul_f32_e32 v53, 0xbf38aa3b, v81
	v_pk_fma_f32 v[92:93], v[78:79], v[92:93], s[34:35] op_sel_hi:[1,1,0]
	v_exp_f32_e32 v81, v53
	v_pk_fma_f32 v[92:93], v[78:79], v[92:93], s[40:41] op_sel_hi:[1,1,0]
	v_and_b32_e32 v77, 0x7fffffff, v73
	v_and_b32_e32 v76, 0x7fffffff, v72
	v_pk_mul_f32 v[78:79], v[78:79], v[92:93]
	v_readlane_b32 s0, v52, 3
	v_max_f32_e32 v72, 0, v72
	v_max_f32_e32 v73, 0, v73
	v_pk_mul_f32 v[76:77], v[76:77], v[78:79]
	v_pk_mul_f32 v[70:71], s[0:1], v[70:71] op_sel_hi:[0,1]
	v_pk_fma_f32 v[72:73], v[80:81], v[76:77], v[72:73] neg_lo:[1,0,0] neg_hi:[1,0,0]
	v_pk_fma_f32 v[70:71], v[70:71], v[238:239], v[242:243]
	v_cvt_pk_f16_f32 v74, v74, v75
	v_cvt_pk_f16_f32 v75, v72, v73
	v_fma_f32 v53, |v70|, s25, 1.0
	ds_write_b64 v135, v[74:75] offset:33792
	v_rcp_f32_e32 v74, v53
	v_fma_f32 v53, |v71|, s25, 1.0
	v_rcp_f32_e32 v75, v53
	v_pk_mul_f32 v[76:77], v[70:71], v[70:71]
	v_pk_mul_f32 v[68:69], s[0:1], v[68:69] op_sel_hi:[0,1]
	v_mul_f32_e32 v53, 0xbf38aa3b, v76
	v_pk_fma_f32 v[78:79], v[74:75], s[22:23], v[90:91] op_sel_hi:[1,0,0]
	v_exp_f32_e32 v76, v53
	v_pk_fma_f32 v[78:79], v[74:75], v[78:79], s[24:25] op_sel_hi:[1,1,0]
	v_mul_f32_e32 v53, 0xbf38aa3b, v77
	v_pk_fma_f32 v[78:79], v[74:75], v[78:79], s[34:35] op_sel_hi:[1,1,0]
	v_pk_fma_f32 v[68:69], v[68:69], v[240:241], v[244:245]
	v_pk_fma_f32 v[78:79], v[74:75], v[78:79], s[40:41] op_sel_hi:[1,1,0]
	v_and_b32_e32 v73, 0x7fffffff, v71
	v_and_b32_e32 v72, 0x7fffffff, v70
	v_exp_f32_e32 v77, v53
	v_pk_mul_f32 v[74:75], v[74:75], v[78:79]
	v_fma_f32 v53, |v68|, s25, 1.0
	v_pk_mul_f32 v[72:73], v[72:73], v[74:75]
	v_rcp_f32_e32 v74, v53
	v_fma_f32 v53, |v69|, s25, 1.0
	v_rcp_f32_e32 v75, v53
	v_max_f32_e32 v70, 0, v70
	v_max_f32_e32 v71, 0, v71
	v_pk_fma_f32 v[70:71], v[76:77], v[72:73], v[70:71] neg_lo:[1,0,0] neg_hi:[1,0,0]
	v_pk_mul_f32 v[76:77], v[68:69], v[68:69]
	v_pk_fma_f32 v[78:79], v[74:75], s[22:23], v[90:91] op_sel_hi:[1,0,0]
	v_mul_f32_e32 v53, 0xbf38aa3b, v76
	v_exp_f32_e32 v76, v53
	v_pk_fma_f32 v[78:79], v[74:75], v[78:79], s[24:25] op_sel_hi:[1,1,0]
	v_mul_f32_e32 v53, 0xbf38aa3b, v77
	v_pk_fma_f32 v[78:79], v[74:75], v[78:79], s[34:35] op_sel_hi:[1,1,0]
	v_exp_f32_e32 v77, v53
	v_pk_fma_f32 v[78:79], v[74:75], v[78:79], s[40:41] op_sel_hi:[1,1,0]
	v_and_b32_e32 v73, 0x7fffffff, v69
	v_and_b32_e32 v72, 0x7fffffff, v68
	v_pk_mul_f32 v[74:75], v[74:75], v[78:79]
	v_readlane_b32 s0, v52, 4
	v_max_f32_e32 v68, 0, v68
	v_max_f32_e32 v69, 0, v69
	v_pk_mul_f32 v[72:73], v[72:73], v[74:75]
	v_pk_mul_f32 v[66:67], s[0:1], v[66:67] op_sel_hi:[0,1]
	v_pk_fma_f32 v[68:69], v[76:77], v[72:73], v[68:69] neg_lo:[1,0,0] neg_hi:[1,0,0]
	v_pk_fma_f32 v[66:67], v[66:67], v[238:239], v[242:243]
	v_cvt_pk_f16_f32 v70, v70, v71
	v_cvt_pk_f16_f32 v71, v68, v69
	v_fma_f32 v53, |v66|, s25, 1.0
	ds_write_b64 v134, v[70:71] offset:34304
	v_rcp_f32_e32 v70, v53
	v_fma_f32 v53, |v67|, s25, 1.0
	v_rcp_f32_e32 v71, v53
	v_pk_mul_f32 v[72:73], v[66:67], v[66:67]
	v_pk_mul_f32 v[64:65], s[0:1], v[64:65] op_sel_hi:[0,1]
	v_mul_f32_e32 v53, 0xbf38aa3b, v72
	v_pk_fma_f32 v[74:75], v[70:71], s[22:23], v[90:91] op_sel_hi:[1,0,0]
	v_exp_f32_e32 v72, v53
	v_pk_fma_f32 v[74:75], v[70:71], v[74:75], s[24:25] op_sel_hi:[1,1,0]
	v_mul_f32_e32 v53, 0xbf38aa3b, v73
	v_pk_fma_f32 v[74:75], v[70:71], v[74:75], s[34:35] op_sel_hi:[1,1,0]
	v_pk_fma_f32 v[64:65], v[64:65], v[240:241], v[244:245]
	v_pk_fma_f32 v[74:75], v[70:71], v[74:75], s[40:41] op_sel_hi:[1,1,0]
	v_and_b32_e32 v69, 0x7fffffff, v67
	v_and_b32_e32 v68, 0x7fffffff, v66
	v_exp_f32_e32 v73, v53
	v_pk_mul_f32 v[70:71], v[70:71], v[74:75]
	v_fma_f32 v53, |v64|, s25, 1.0
	v_pk_mul_f32 v[68:69], v[68:69], v[70:71]
	v_rcp_f32_e32 v70, v53
	v_fma_f32 v53, |v65|, s25, 1.0
	v_rcp_f32_e32 v71, v53
	v_max_f32_e32 v66, 0, v66
	v_max_f32_e32 v67, 0, v67
	v_pk_fma_f32 v[66:67], v[72:73], v[68:69], v[66:67] neg_lo:[1,0,0] neg_hi:[1,0,0]
	v_pk_mul_f32 v[72:73], v[64:65], v[64:65]
	v_pk_fma_f32 v[74:75], v[70:71], s[22:23], v[90:91] op_sel_hi:[1,0,0]
	v_mul_f32_e32 v53, 0xbf38aa3b, v72
	v_exp_f32_e32 v72, v53
	v_pk_fma_f32 v[74:75], v[70:71], v[74:75], s[24:25] op_sel_hi:[1,1,0]
	v_mul_f32_e32 v53, 0xbf38aa3b, v73
	v_pk_fma_f32 v[74:75], v[70:71], v[74:75], s[34:35] op_sel_hi:[1,1,0]
	v_exp_f32_e32 v73, v53
	v_pk_fma_f32 v[74:75], v[70:71], v[74:75], s[40:41] op_sel_hi:[1,1,0]
	v_and_b32_e32 v69, 0x7fffffff, v65
	v_and_b32_e32 v68, 0x7fffffff, v64
	v_pk_mul_f32 v[70:71], v[70:71], v[74:75]
	v_readlane_b32 s0, v52, 5
	v_max_f32_e32 v64, 0, v64
	v_max_f32_e32 v65, 0, v65
	v_pk_mul_f32 v[68:69], v[68:69], v[70:71]
	v_pk_mul_f32 v[62:63], s[0:1], v[62:63] op_sel_hi:[0,1]
	v_pk_fma_f32 v[64:65], v[72:73], v[68:69], v[64:65] neg_lo:[1,0,0] neg_hi:[1,0,0]
	v_pk_fma_f32 v[62:63], v[62:63], v[238:239], v[242:243]
	v_cvt_pk_f16_f32 v66, v66, v67
	v_cvt_pk_f16_f32 v67, v64, v65
	v_fma_f32 v53, |v62|, s25, 1.0
	ds_write_b64 v120, v[66:67] offset:34816
	v_rcp_f32_e32 v66, v53
	v_fma_f32 v53, |v63|, s25, 1.0
	v_rcp_f32_e32 v67, v53
	v_pk_mul_f32 v[68:69], v[62:63], v[62:63]
	v_pk_mul_f32 v[60:61], s[0:1], v[60:61] op_sel_hi:[0,1]
	v_mul_f32_e32 v53, 0xbf38aa3b, v68
	v_pk_fma_f32 v[70:71], v[66:67], s[22:23], v[90:91] op_sel_hi:[1,0,0]
	v_exp_f32_e32 v68, v53
	v_pk_fma_f32 v[70:71], v[66:67], v[70:71], s[24:25] op_sel_hi:[1,1,0]
	v_mul_f32_e32 v53, 0xbf38aa3b, v69
	v_pk_fma_f32 v[70:71], v[66:67], v[70:71], s[34:35] op_sel_hi:[1,1,0]
	v_pk_fma_f32 v[60:61], v[60:61], v[240:241], v[244:245]
	v_pk_fma_f32 v[70:71], v[66:67], v[70:71], s[40:41] op_sel_hi:[1,1,0]
	v_and_b32_e32 v65, 0x7fffffff, v63
	v_and_b32_e32 v64, 0x7fffffff, v62
	v_exp_f32_e32 v69, v53
	v_pk_mul_f32 v[66:67], v[66:67], v[70:71]
	v_fma_f32 v53, |v60|, s25, 1.0
	v_pk_mul_f32 v[64:65], v[64:65], v[66:67]
	v_rcp_f32_e32 v66, v53
	v_fma_f32 v53, |v61|, s25, 1.0
	v_rcp_f32_e32 v67, v53
	v_max_f32_e32 v62, 0, v62
	v_max_f32_e32 v63, 0, v63
	v_pk_fma_f32 v[62:63], v[68:69], v[64:65], v[62:63] neg_lo:[1,0,0] neg_hi:[1,0,0]
	v_pk_mul_f32 v[68:69], v[60:61], v[60:61]
	v_pk_fma_f32 v[70:71], v[66:67], s[22:23], v[90:91] op_sel_hi:[1,0,0]
	v_mul_f32_e32 v53, 0xbf38aa3b, v68
	v_exp_f32_e32 v68, v53
	v_pk_fma_f32 v[70:71], v[66:67], v[70:71], s[24:25] op_sel_hi:[1,1,0]
	v_mul_f32_e32 v53, 0xbf38aa3b, v69
	v_pk_fma_f32 v[70:71], v[66:67], v[70:71], s[34:35] op_sel_hi:[1,1,0]
	v_exp_f32_e32 v69, v53
	v_pk_fma_f32 v[70:71], v[66:67], v[70:71], s[40:41] op_sel_hi:[1,1,0]
	v_and_b32_e32 v65, 0x7fffffff, v61
	v_and_b32_e32 v64, 0x7fffffff, v60
	v_pk_mul_f32 v[66:67], v[66:67], v[70:71]
	v_readlane_b32 s0, v52, 6
	v_max_f32_e32 v60, 0, v60
	v_max_f32_e32 v61, 0, v61
	v_pk_mul_f32 v[64:65], v[64:65], v[66:67]
	v_pk_mul_f32 v[58:59], s[0:1], v[58:59] op_sel_hi:[0,1]
	v_pk_fma_f32 v[60:61], v[68:69], v[64:65], v[60:61] neg_lo:[1,0,0] neg_hi:[1,0,0]
	v_pk_fma_f32 v[58:59], v[58:59], v[238:239], v[242:243]
	v_cvt_pk_f16_f32 v62, v62, v63
	v_cvt_pk_f16_f32 v63, v60, v61
	v_fma_f32 v53, |v58|, s25, 1.0
	ds_write_b64 v121, v[62:63] offset:35328
	v_rcp_f32_e32 v62, v53
	v_fma_f32 v53, |v59|, s25, 1.0
	v_rcp_f32_e32 v63, v53
	v_pk_mul_f32 v[64:65], v[58:59], v[58:59]
	v_pk_mul_f32 v[56:57], s[0:1], v[56:57] op_sel_hi:[0,1]
	v_mul_f32_e32 v53, 0xbf38aa3b, v64
	v_pk_fma_f32 v[66:67], v[62:63], s[22:23], v[90:91] op_sel_hi:[1,0,0]
	v_exp_f32_e32 v64, v53
	v_pk_fma_f32 v[66:67], v[62:63], v[66:67], s[24:25] op_sel_hi:[1,1,0]
	v_mul_f32_e32 v53, 0xbf38aa3b, v65
	v_pk_fma_f32 v[66:67], v[62:63], v[66:67], s[34:35] op_sel_hi:[1,1,0]
	v_pk_fma_f32 v[56:57], v[56:57], v[240:241], v[244:245]
	v_pk_fma_f32 v[66:67], v[62:63], v[66:67], s[40:41] op_sel_hi:[1,1,0]
	v_and_b32_e32 v61, 0x7fffffff, v59
	v_and_b32_e32 v60, 0x7fffffff, v58
	v_exp_f32_e32 v65, v53
	v_pk_mul_f32 v[62:63], v[62:63], v[66:67]
	v_fma_f32 v53, |v56|, s25, 1.0
	v_pk_mul_f32 v[60:61], v[60:61], v[62:63]
	v_rcp_f32_e32 v62, v53
	v_fma_f32 v53, |v57|, s25, 1.0
	v_rcp_f32_e32 v63, v53
	v_max_f32_e32 v58, 0, v58
	v_max_f32_e32 v59, 0, v59
	v_pk_fma_f32 v[58:59], v[64:65], v[60:61], v[58:59] neg_lo:[1,0,0] neg_hi:[1,0,0]
	v_pk_mul_f32 v[64:65], v[56:57], v[56:57]
	v_pk_fma_f32 v[66:67], v[62:63], s[22:23], v[90:91] op_sel_hi:[1,0,0]
	v_mul_f32_e32 v53, 0xbf38aa3b, v64
	v_exp_f32_e32 v64, v53
	v_pk_fma_f32 v[66:67], v[62:63], v[66:67], s[24:25] op_sel_hi:[1,1,0]
	v_mul_f32_e32 v53, 0xbf38aa3b, v65
	v_pk_fma_f32 v[66:67], v[62:63], v[66:67], s[34:35] op_sel_hi:[1,1,0]
	v_exp_f32_e32 v65, v53
	v_pk_fma_f32 v[66:67], v[62:63], v[66:67], s[40:41] op_sel_hi:[1,1,0]
	v_and_b32_e32 v61, 0x7fffffff, v57
	v_and_b32_e32 v60, 0x7fffffff, v56
	v_pk_mul_f32 v[62:63], v[62:63], v[66:67]
	v_readlane_b32 s0, v52, 7
	v_max_f32_e32 v56, 0, v56
	v_max_f32_e32 v57, 0, v57
	v_pk_mul_f32 v[60:61], v[60:61], v[62:63]
	v_pk_mul_f32 v[52:53], s[0:1], v[54:55] op_sel_hi:[0,1]
	v_pk_fma_f32 v[56:57], v[64:65], v[60:61], v[56:57] neg_lo:[1,0,0] neg_hi:[1,0,0]
	v_pk_fma_f32 v[52:53], v[52:53], v[238:239], v[242:243]
	v_cvt_pk_f16_f32 v58, v58, v59
	v_cvt_pk_f16_f32 v59, v56, v57
	v_fma_f32 v56, |v52|, s25, 1.0
	v_fma_f32 v57, |v53|, s25, 1.0
	v_rcp_f32_e32 v56, v56
	v_rcp_f32_e32 v57, v57
	ds_write_b64 v118, v[58:59] offset:35840
	v_pk_mul_f32 v[58:59], v[52:53], v[52:53]
	v_and_b32_e32 v55, 0x7fffffff, v53
	v_pk_fma_f32 v[60:61], v[56:57], s[22:23], v[90:91] op_sel_hi:[1,0,0]
	v_mul_f32_e32 v58, 0xbf38aa3b, v58
	v_pk_fma_f32 v[60:61], v[56:57], v[60:61], s[24:25] op_sel_hi:[1,1,0]
	v_mul_f32_e32 v59, 0xbf38aa3b, v59
	v_exp_f32_e32 v58, v58
	v_pk_fma_f32 v[60:61], v[56:57], v[60:61], s[34:35] op_sel_hi:[1,1,0]
	v_exp_f32_e32 v59, v59
	v_pk_fma_f32 v[60:61], v[56:57], v[60:61], s[40:41] op_sel_hi:[1,1,0]
	v_and_b32_e32 v54, 0x7fffffff, v52
	v_pk_mul_f32 v[56:57], v[56:57], v[60:61]
	v_max_f32_e32 v52, 0, v52
	v_max_f32_e32 v53, 0, v53
	v_pk_mul_f32 v[54:55], v[54:55], v[56:57]
	v_pk_mul_f32 v[50:51], s[0:1], v[50:51] op_sel_hi:[0,1]
	v_pk_fma_f32 v[52:53], v[58:59], v[54:55], v[52:53] neg_lo:[1,0,0] neg_hi:[1,0,0]
	v_pk_fma_f32 v[50:51], v[50:51], v[240:241], v[244:245]
	v_cvt_pk_f16_f32 v52, v52, v53
	v_fma_f32 v53, |v50|, s25, 1.0
	v_rcp_f32_e32 v56, v53
	v_fma_f32 v53, |v51|, s25, 1.0
	v_rcp_f32_e32 v57, v53
	v_pk_mul_f32 v[58:59], v[50:51], v[50:51]
	v_and_b32_e32 v55, 0x7fffffff, v51
	v_mul_f32_e32 v53, 0xbf38aa3b, v58
	v_pk_fma_f32 v[60:61], v[56:57], s[22:23], v[90:91] op_sel_hi:[1,0,0]
	v_exp_f32_e32 v58, v53
	v_pk_fma_f32 v[60:61], v[56:57], v[60:61], s[24:25] op_sel_hi:[1,1,0]
	v_mul_f32_e32 v53, 0xbf38aa3b, v59
	v_pk_fma_f32 v[60:61], v[56:57], v[60:61], s[34:35] op_sel_hi:[1,1,0]
	v_exp_f32_e32 v59, v53
	v_pk_fma_f32 v[60:61], v[56:57], v[60:61], s[40:41] op_sel_hi:[1,1,0]
	v_and_b32_e32 v54, 0x7fffffff, v50
	v_pk_mul_f32 v[56:57], v[56:57], v[60:61]
	v_max_f32_e32 v50, 0, v50
	v_max_f32_e32 v51, 0, v51
	v_pk_mul_f32 v[54:55], v[54:55], v[56:57]
	s_movk_i32 s0, 0x70
	v_pk_fma_f32 v[50:51], v[58:59], v[54:55], v[50:51] neg_lo:[1,0,0] neg_hi:[1,0,0]
	s_waitcnt vmcnt(0)
	v_add_f32_e32 v96, v24, v25
	v_cvt_pk_f16_f32 v53, v50, v51
	v_bitop3_b32 v50, v86, s0, v88 bitop3:0x6c
	s_movk_i32 s0, 0x4000
	v_add_co_u32_e32 v92, vcc, s0, v82
	s_movk_i32 s0, 0x5000
	s_nop 0
	v_addc_co_u32_e32 v93, vcc, 0, v83, vcc
	v_or3_b32 v144, v85, v50, v87
	v_add_co_u32_e32 v94, vcc, s0, v82
	ds_write_b64 v144, v[52:53] offset:36352
	s_nop 0
	v_addc_co_u32_e32 v95, vcc, 0, v83, vcc
	s_movk_i32 s56, 0x5000
	v_add_co_u32_e64 v234, s[58:59], s56, v82
	s_nop 1
	v_addc_co_u32_e64 v235, s[58:59], 0, v83, s[58:59]
	global_load_dwordx4 v[170:173], v[234:235], off offset:-4096 nt
	global_load_dwordx4 v[174:177], v[234:235], off offset:-3072 nt
	global_load_dwordx4 v[178:181], v[234:235], off offset:-2048 nt
	global_load_dwordx4 v[182:185], v[234:235], off offset:-1024 nt
	global_load_dwordx4 v[186:189], v[234:235], off nt
	global_load_dwordx4 v[190:193], v[234:235], off offset:1024 nt
	global_load_dwordx4 v[194:197], v[234:235], off offset:2048 nt
	global_load_dwordx4 v[198:201], v[234:235], off offset:3072 nt
	v_add_f32_e32 v92, v40, v41
	v_add_f32_e32 v89, v89, v92
	v_add_f32_e32 v92, v34, v35
	v_add_f32_e32 v93, v36, v37
	v_add_f32_e32 v92, v92, v93
	v_add_f32_e32 v93, v30, v31
	v_add_f32_e32 v94, v32, v33
	v_add_f32_e32 v93, v93, v94
	v_add_f32_e32 v94, v26, v27
	v_add_f32_e32 v95, v28, v29
	v_add_f32_e32 v94, v94, v95
	v_add_f32_e32 v95, v22, v23
	v_add_f32_e32 v95, v95, v96
	v_add_f32_e32 v96, v18, v19
	v_add_f32_e32 v97, v20, v21
	v_add_f32_e32 v96, v96, v97
	v_add_f32_e32 v97, v14, v15
	v_add_f32_e32 v98, v16, v17
	v_add_f32_e32 v97, v97, v98
	v_add_f32_e32 v98, v10, v11
	v_add_f32_e32 v99, v12, v13
	v_add_f32_e32 v98, v98, v99
	v_cndmask_b32_e64 v99, v92, v89, s[4:5]
	v_cndmask_b32_e64 v89, v89, v92, s[4:5]
	v_cndmask_b32_e64 v92, v94, v93, s[4:5]
	v_cndmask_b32_e64 v93, v93, v94, s[4:5]
	v_cndmask_b32_e64 v94, v95, v96, s[4:5]
	v_add_f32_dpp v89, v99, v89 quad_perm:[1,0,3,2] row_mask:0xf bank_mask:0xf bound_ctrl:1
	v_add_f32_dpp v92, v92, v93 quad_perm:[1,0,3,2] row_mask:0xf bank_mask:0xf bound_ctrl:1
	v_cndmask_b32_e64 v93, v96, v95, s[4:5]
	v_cndmask_b32_e64 v95, v97, v98, s[4:5]
	s_movk_i32 s1, 0x80
	v_add_f32_dpp v93, v93, v94 quad_perm:[1,0,3,2] row_mask:0xf bank_mask:0xf bound_ctrl:1
	v_cndmask_b32_e64 v94, v98, v97, s[4:5]
	s_movk_i32 s23, 0x90
	s_nop 0
	v_add_f32_dpp v94, v94, v95 quad_perm:[1,0,3,2] row_mask:0xf bank_mask:0xf bound_ctrl:1
	v_cndmask_b32_e64 v95, v89, v92, s[6:7]
	v_cndmask_b32_e64 v89, v92, v89, s[6:7]
	v_cndmask_b32_e64 v92, v93, v94, s[6:7]
	v_cndmask_b32_e64 v93, v94, v93, s[6:7]
	v_add_f32_dpp v89, v95, v89 quad_perm:[2,3,0,1] row_mask:0xf bank_mask:0xf bound_ctrl:1
	s_nop 0
	v_add_f32_dpp v92, v92, v93 quad_perm:[2,3,0,1] row_mask:0xf bank_mask:0xf bound_ctrl:1
	v_cndmask_b32_e64 v93, v89, v92, s[8:9]
	v_cndmask_b32_e64 v89, v92, v89, s[8:9]
	v_mov_b32_e32 v92, v93
	s_nop 1
	v_mov_b32_dpp v92, v92 row_shl:4 row_mask:0xf bank_mask:0x5
	s_nop 1
	v_mov_b32_dpp v92, v93 row_shr:4 row_mask:0xf bank_mask:0xa
	v_add_f32_e32 v89, v89, v92
	s_nop 1
	v_add_f32_dpp v89, v89, v89 row_ror:8 row_mask:0xf bank_mask:0xf bound_ctrl:1
	v_mov_b32_e32 v92, v89
	s_nop 1
	v_permlane16_swap_b32_e32 v89, v92
	v_add_f32_e32 v89, v89, v92
	v_mov_b32_e32 v92, v89
	s_nop 1
	v_permlane32_swap_b32_e32 v89, v92
	v_add_f32_e32 v89, v89, v92
	v_mul_f32_e32 v89, 0x3b800000, v89
	v_bitop3_b32 v92, v86, s1, v88 bitop3:0x6c
	v_readlane_b32 s44, v89, 0
	v_readlane_b32 s46, v89, 1
	v_readlane_b32 s48, v89, 2
	v_pk_add_f32 v[40:41], v[40:41], s[44:45] op_sel_hi:[1,0] neg_lo:[0,1] neg_hi:[0,1]
	v_pk_add_f32 v[36:37], v[36:37], s[46:47] op_sel_hi:[1,0] neg_lo:[0,1] neg_hi:[0,1]
	v_readlane_b32 s50, v89, 3
	v_readlane_b32 s52, v89, 4
	v_readlane_b32 s54, v89, 5
	v_readlane_b32 s42, v89, 6
	v_readlane_b32 s0, v89, 7
	v_mul_f32_e32 v89, v41, v41
	v_or3_b32 v145, v85, v92, v87
	v_pk_add_f32 v[92:93], v[34:35], s[46:47] op_sel_hi:[1,0] neg_lo:[0,1] neg_hi:[0,1]
	v_mul_f32_e32 v34, v37, v37
	v_pk_add_f32 v[38:39], v[38:39], s[44:45] op_sel_hi:[1,0] neg_lo:[0,1] neg_hi:[0,1]
	v_fmac_f32_e32 v89, v40, v40
	v_fmac_f32_e32 v34, v36, v36
	v_fmac_f32_e32 v89, v39, v39
	v_fmac_f32_e32 v34, v93, v93
	v_fmac_f32_e32 v89, v38, v38
	v_fmac_f32_e32 v34, v92, v92
	v_cndmask_b32_e64 v35, v34, v89, s[4:5]
	v_cndmask_b32_e64 v34, v89, v34, s[4:5]
	s_movk_i32 s1, 0xa0
	v_pk_add_f32 v[32:33], v[32:33], s[48:49] op_sel_hi:[1,0] neg_lo:[0,1] neg_hi:[0,1]
	v_add_f32_dpp v89, v35, v34 quad_perm:[1,0,3,2] row_mask:0xf bank_mask:0xf bound_ctrl:1
	v_bitop3_b32 v34, v86, s23, v88 bitop3:0x6c
	v_or3_b32 v139, v85, v34, v87
	v_pk_add_f32 v[34:35], v[30:31], s[48:49] op_sel_hi:[1,0] neg_lo:[0,1] neg_hi:[0,1]
	v_bitop3_b32 v30, v86, s1, v88 bitop3:0x6c
	v_pk_add_f32 v[28:29], v[28:29], s[50:51] op_sel_hi:[1,0] neg_lo:[0,1] neg_hi:[0,1]
	v_mul_f32_e32 v94, v33, v33
	v_or3_b32 v137, v85, v30, v87
	v_pk_add_f32 v[30:31], v[26:27], s[50:51] op_sel_hi:[1,0] neg_lo:[0,1] neg_hi:[0,1]
	v_mul_f32_e32 v26, v29, v29
	v_fmac_f32_e32 v94, v32, v32
	v_fmac_f32_e32 v26, v28, v28
	v_fmac_f32_e32 v94, v35, v35
	v_fmac_f32_e32 v26, v31, v31
	v_fmac_f32_e32 v94, v34, v34
	v_fmac_f32_e32 v26, v30, v30
	v_cndmask_b32_e64 v27, v26, v94, s[4:5]
	v_cndmask_b32_e64 v26, v94, v26, s[4:5]
	s_movk_i32 s1, 0xb0
	v_pk_add_f32 v[24:25], v[24:25], s[52:53] op_sel_hi:[1,0] neg_lo:[0,1] neg_hi:[0,1]
	v_add_f32_dpp v26, v27, v26 quad_perm:[1,0,3,2] row_mask:0xf bank_mask:0xf bound_ctrl:1
	v_cndmask_b32_e64 v27, v89, v26, s[6:7]
	v_cndmask_b32_e64 v26, v26, v89, s[6:7]
	v_pk_add_f32 v[20:21], v[20:21], s[54:55] op_sel_hi:[1,0] neg_lo:[0,1] neg_hi:[0,1]
	v_mul_f32_e32 v94, v25, v25
	v_add_f32_dpp v89, v27, v26 quad_perm:[2,3,0,1] row_mask:0xf bank_mask:0xf bound_ctrl:1
	v_bitop3_b32 v26, v86, s1, v88 bitop3:0x6c
	s_movk_i32 s1, 0xc0
	v_or3_b32 v136, v85, v26, v87
	v_pk_add_f32 v[26:27], v[22:23], s[52:53] op_sel_hi:[1,0] neg_lo:[0,1] neg_hi:[0,1]
	v_bitop3_b32 v22, v86, s1, v88 bitop3:0x6c
	v_or3_b32 v123, v85, v22, v87
	v_pk_add_f32 v[22:23], v[18:19], s[54:55] op_sel_hi:[1,0] neg_lo:[0,1] neg_hi:[0,1]
	v_mul_f32_e32 v18, v21, v21
	v_fmac_f32_e32 v94, v24, v24
	v_fmac_f32_e32 v18, v20, v20
	v_fmac_f32_e32 v94, v27, v27
	v_fmac_f32_e32 v18, v23, v23
	v_fmac_f32_e32 v94, v26, v26
	v_fmac_f32_e32 v18, v22, v22
	v_cndmask_b32_e64 v19, v18, v94, s[4:5]
	v_cndmask_b32_e64 v18, v94, v18, s[4:5]
	v_pk_add_f32 v[16:17], v[16:17], s[42:43] op_sel_hi:[1,0] neg_lo:[0,1] neg_hi:[0,1]
	s_nop 0
	v_add_f32_dpp v94, v19, v18 quad_perm:[1,0,3,2] row_mask:0xf bank_mask:0xf bound_ctrl:1
	v_pk_add_f32 v[18:19], v[14:15], s[42:43] op_sel_hi:[1,0] neg_lo:[0,1] neg_hi:[0,1]
	v_pk_add_f32 v[14:15], v[10:11], s[0:1] op_sel_hi:[1,0] neg_lo:[0,1] neg_hi:[0,1]
	v_pk_add_f32 v[10:11], v[12:13], s[0:1] op_sel_hi:[1,0] neg_lo:[0,1] neg_hi:[0,1]
	v_mul_f32_e32 v95, v17, v17
	v_mul_f32_e32 v12, v11, v11
	v_fmac_f32_e32 v95, v16, v16
	v_fmac_f32_e32 v12, v10, v10
	v_fmac_f32_e32 v95, v19, v19
	v_fmac_f32_e32 v12, v15, v15
	v_fmac_f32_e32 v95, v18, v18
	v_fmac_f32_e32 v12, v14, v14
	v_cndmask_b32_e64 v13, v12, v95, s[4:5]
	v_cndmask_b32_e64 v12, v95, v12, s[4:5]
	s_movk_i32 s0, 0xd0
	s_nop 0
	v_add_f32_dpp v12, v13, v12 quad_perm:[1,0,3,2] row_mask:0xf bank_mask:0xf bound_ctrl:1
	v_cndmask_b32_e64 v13, v94, v12, s[6:7]
	v_cndmask_b32_e64 v12, v12, v94, s[6:7]
	s_nop 1
	v_add_f32_dpp v12, v13, v12 quad_perm:[2,3,0,1] row_mask:0xf bank_mask:0xf bound_ctrl:1
	v_cndmask_b32_e64 v13, v89, v12, s[8:9]
	v_cndmask_b32_e64 v12, v12, v89, s[8:9]
	v_mov_b32_e32 v89, v13
	s_nop 1
	v_mov_b32_dpp v89, v89 row_shl:4 row_mask:0xf bank_mask:0x5
	s_nop 1
	v_mov_b32_dpp v89, v13 row_shr:4 row_mask:0xf bank_mask:0xa
	v_add_f32_e32 v12, v12, v89
	v_bitop3_b32 v89, v86, s0, v88 bitop3:0x6c
	v_or3_b32 v133, v85, v89, v87
	v_add_f32_dpp v12, v12, v12 row_ror:8 row_mask:0xf bank_mask:0xf bound_ctrl:1
	v_mov_b32_e32 v13, v12
	s_nop 1
	v_permlane16_swap_b32_e32 v12, v13
	v_add_f32_e32 v12, v12, v13
	v_mov_b32_e32 v13, v12
	s_nop 1
	v_permlane32_swap_b32_e32 v12, v13
	v_add_f32_e32 v12, v12, v13
	v_fmamk_f32 v12, v12, 0x3b800000, v116
	v_mul_f32_e32 v13, 0x4f800000, v12
	v_cmp_gt_f32_e32 vcc, s35, v12
	s_nop 1
	v_cndmask_b32_e32 v12, v12, v13, vcc
	v_sqrt_f32_e32 v13, v12
	s_nop 0
	v_add_u32_e32 v89, -1, v13
	v_fma_f32 v94, -v89, v13, v12
	v_cmp_ge_f32_e64 s[0:1], 0, v94
	v_add_u32_e32 v94, 1, v13
	s_nop 0
	v_cndmask_b32_e64 v89, v13, v89, s[0:1]
	v_fma_f32 v13, -v94, v13, v12
	v_cmp_lt_f32_e64 s[0:1], 0, v13
	s_nop 1
	v_cndmask_b32_e64 v13, v89, v94, s[0:1]
	v_mul_f32_e32 v89, 0x37800000, v13
	v_cndmask_b32_e32 v13, v13, v89, vcc
	v_cmp_class_f32_e32 vcc, v12, v117
	s_nop 1
	v_cndmask_b32_e32 v12, v13, v12, vcc
	v_div_scale_f32 v13, s[0:1], v12, v12, 1.0
	v_rcp_f32_e32 v89, v13
	s_movk_i32 s0, 0xe0
	v_bitop3_b32 v94, v86, s0, v88 bitop3:0x6c
	v_or3_b32 v119, v85, v94, v87
	v_fma_f32 v94, -v13, v89, 1.0
	v_fmac_f32_e32 v89, v94, v89
	v_div_scale_f32 v94, vcc, 1.0, v12, 1.0
	v_mul_f32_e32 v95, v94, v89
	v_fma_f32 v96, -v13, v95, v94
	v_fmac_f32_e32 v95, v96, v89
	v_fma_f32 v13, -v13, v95, v94
	v_div_fmas_f32 v13, v13, v89, v95
	v_div_fixup_f32 v12, v13, v12, 1.0
	s_nop 0
	v_readlane_b32 s0, v12, 0
	s_nop 1
	v_pk_mul_f32 v[38:39], s[0:1], v[38:39] op_sel_hi:[0,1]
	v_pk_fma_f32 v[38:39], v[38:39], v[238:239], v[242:243]
	v_pk_mul_f32 v[40:41], s[0:1], v[40:41] op_sel_hi:[0,1]
	v_fma_f32 v13, |v38|, s25, 1.0
	v_rcp_f32_e32 v96, v13
	v_fma_f32 v13, |v39|, s25, 1.0
	v_rcp_f32_e32 v97, v13
	v_pk_mul_f32 v[98:99], v[38:39], v[38:39]
	v_pk_fma_f32 v[40:41], v[40:41], v[240:241], v[244:245]
	v_mul_f32_e32 v13, 0xbf38aa3b, v98
	v_pk_fma_f32 v[100:101], v[96:97], s[22:23], v[90:91] op_sel_hi:[1,0,0]
	v_exp_f32_e32 v98, v13
	v_pk_fma_f32 v[100:101], v[96:97], v[100:101], s[24:25] op_sel_hi:[1,1,0]
	v_mul_f32_e32 v13, 0xbf38aa3b, v99
	v_pk_fma_f32 v[100:101], v[96:97], v[100:101], s[34:35] op_sel_hi:[1,1,0]
	v_and_b32_e32 v95, 0x7fffffff, v39
	v_pk_fma_f32 v[100:101], v[96:97], v[100:101], s[40:41] op_sel_hi:[1,1,0]
	v_and_b32_e32 v94, 0x7fffffff, v38
	v_exp_f32_e32 v99, v13
	v_pk_mul_f32 v[96:97], v[96:97], v[100:101]
	v_fma_f32 v13, |v40|, s25, 1.0
	v_pk_mul_f32 v[94:95], v[94:95], v[96:97]
	v_rcp_f32_e32 v96, v13
	v_fma_f32 v13, |v41|, s25, 1.0
	v_rcp_f32_e32 v97, v13
	v_max_f32_e32 v38, 0, v38
	v_max_f32_e32 v39, 0, v39
	v_pk_fma_f32 v[38:39], v[98:99], v[94:95], v[38:39] neg_lo:[1,0,0] neg_hi:[1,0,0]
	v_pk_mul_f32 v[98:99], v[40:41], v[40:41]
	v_pk_fma_f32 v[100:101], v[96:97], s[22:23], v[90:91] op_sel_hi:[1,0,0]
	v_mul_f32_e32 v13, 0xbf38aa3b, v98
	v_exp_f32_e32 v98, v13
	v_pk_fma_f32 v[100:101], v[96:97], v[100:101], s[24:25] op_sel_hi:[1,1,0]
	v_mul_f32_e32 v13, 0xbf38aa3b, v99
	v_pk_fma_f32 v[100:101], v[96:97], v[100:101], s[34:35] op_sel_hi:[1,1,0]
	v_exp_f32_e32 v99, v13
	v_pk_fma_f32 v[100:101], v[96:97], v[100:101], s[40:41] op_sel_hi:[1,1,0]
	v_and_b32_e32 v95, 0x7fffffff, v41
	v_and_b32_e32 v94, 0x7fffffff, v40
	v_pk_mul_f32 v[96:97], v[96:97], v[100:101]
	v_max_f32_e32 v40, 0, v40
	v_max_f32_e32 v41, 0, v41
	v_pk_mul_f32 v[94:95], v[94:95], v[96:97]
	v_cvt_pk_f16_f32 v38, v38, v39
	v_pk_fma_f32 v[40:41], v[98:99], v[94:95], v[40:41] neg_lo:[1,0,0] neg_hi:[1,0,0]
	v_readlane_b32 s0, v12, 1
	v_cvt_pk_f16_f32 v39, v40, v41
	ds_write_b64 v145, v[38:39] offset:36864
	v_pk_mul_f32 v[38:39], s[0:1], v[92:93] op_sel_hi:[0,1]
	v_pk_fma_f32 v[38:39], v[38:39], v[238:239], v[242:243]
	v_pk_mul_f32 v[36:37], s[0:1], v[36:37] op_sel_hi:[0,1]
	v_fma_f32 v13, |v38|, s25, 1.0
	v_rcp_f32_e32 v92, v13
	v_fma_f32 v13, |v39|, s25, 1.0
	v_rcp_f32_e32 v93, v13
	v_pk_mul_f32 v[94:95], v[38:39], v[38:39]
	v_pk_fma_f32 v[36:37], v[36:37], v[240:241], v[244:245]
	v_mul_f32_e32 v13, 0xbf38aa3b, v94
	v_pk_fma_f32 v[96:97], v[92:93], s[22:23], v[90:91] op_sel_hi:[1,0,0]
	v_exp_f32_e32 v94, v13
	v_pk_fma_f32 v[96:97], v[92:93], v[96:97], s[24:25] op_sel_hi:[1,1,0]
	v_mul_f32_e32 v13, 0xbf38aa3b, v95
	v_pk_fma_f32 v[96:97], v[92:93], v[96:97], s[34:35] op_sel_hi:[1,1,0]
	v_and_b32_e32 v41, 0x7fffffff, v39
	v_pk_fma_f32 v[96:97], v[92:93], v[96:97], s[40:41] op_sel_hi:[1,1,0]
	v_and_b32_e32 v40, 0x7fffffff, v38
	v_exp_f32_e32 v95, v13
	v_pk_mul_f32 v[92:93], v[92:93], v[96:97]
	v_fma_f32 v13, |v36|, s25, 1.0
	v_pk_mul_f32 v[40:41], v[40:41], v[92:93]
	v_rcp_f32_e32 v92, v13
	v_fma_f32 v13, |v37|, s25, 1.0
	v_rcp_f32_e32 v93, v13
	v_max_f32_e32 v38, 0, v38
	v_max_f32_e32 v39, 0, v39
	v_pk_fma_f32 v[38:39], v[94:95], v[40:41], v[38:39] neg_lo:[1,0,0] neg_hi:[1,0,0]
	v_pk_mul_f32 v[94:95], v[36:37], v[36:37]
	v_pk_fma_f32 v[96:97], v[92:93], s[22:23], v[90:91] op_sel_hi:[1,0,0]
	v_mul_f32_e32 v13, 0xbf38aa3b, v94
	v_exp_f32_e32 v94, v13
	v_pk_fma_f32 v[96:97], v[92:93], v[96:97], s[24:25] op_sel_hi:[1,1,0]
	v_mul_f32_e32 v13, 0xbf38aa3b, v95
	v_pk_fma_f32 v[96:97], v[92:93], v[96:97], s[34:35] op_sel_hi:[1,1,0]
	v_exp_f32_e32 v95, v13
	v_pk_fma_f32 v[96:97], v[92:93], v[96:97], s[40:41] op_sel_hi:[1,1,0]
	v_and_b32_e32 v41, 0x7fffffff, v37
	v_and_b32_e32 v40, 0x7fffffff, v36
	v_pk_mul_f32 v[92:93], v[92:93], v[96:97]
	v_readlane_b32 s0, v12, 2
	v_max_f32_e32 v36, 0, v36
	v_max_f32_e32 v37, 0, v37
	v_pk_mul_f32 v[40:41], v[40:41], v[92:93]
	v_pk_mul_f32 v[34:35], s[0:1], v[34:35] op_sel_hi:[0,1]
	v_pk_fma_f32 v[36:37], v[94:95], v[40:41], v[36:37] neg_lo:[1,0,0] neg_hi:[1,0,0]
	v_pk_fma_f32 v[34:35], v[34:35], v[238:239], v[242:243]
	v_cvt_pk_f16_f32 v38, v38, v39
	v_cvt_pk_f16_f32 v39, v36, v37
	v_fma_f32 v13, |v34|, s25, 1.0
	ds_write_b64 v139, v[38:39] offset:37376
	v_rcp_f32_e32 v38, v13
	v_fma_f32 v13, |v35|, s25, 1.0
	v_rcp_f32_e32 v39, v13
	v_pk_mul_f32 v[40:41], v[34:35], v[34:35]
	v_pk_mul_f32 v[32:33], s[0:1], v[32:33] op_sel_hi:[0,1]
	v_mul_f32_e32 v13, 0xbf38aa3b, v40
	v_pk_fma_f32 v[92:93], v[38:39], s[22:23], v[90:91] op_sel_hi:[1,0,0]
	v_exp_f32_e32 v40, v13
	v_pk_fma_f32 v[92:93], v[38:39], v[92:93], s[24:25] op_sel_hi:[1,1,0]
	v_mul_f32_e32 v13, 0xbf38aa3b, v41
	v_pk_fma_f32 v[92:93], v[38:39], v[92:93], s[34:35] op_sel_hi:[1,1,0]
	v_pk_fma_f32 v[32:33], v[32:33], v[240:241], v[244:245]
	v_pk_fma_f32 v[92:93], v[38:39], v[92:93], s[40:41] op_sel_hi:[1,1,0]
	v_and_b32_e32 v37, 0x7fffffff, v35
	v_and_b32_e32 v36, 0x7fffffff, v34
	v_exp_f32_e32 v41, v13
	v_pk_mul_f32 v[38:39], v[38:39], v[92:93]
	v_fma_f32 v13, |v32|, s25, 1.0
	v_pk_mul_f32 v[36:37], v[36:37], v[38:39]
	v_rcp_f32_e32 v38, v13
	v_fma_f32 v13, |v33|, s25, 1.0
	v_rcp_f32_e32 v39, v13
	v_max_f32_e32 v34, 0, v34
	v_max_f32_e32 v35, 0, v35
	v_pk_fma_f32 v[34:35], v[40:41], v[36:37], v[34:35] neg_lo:[1,0,0] neg_hi:[1,0,0]
	v_pk_mul_f32 v[40:41], v[32:33], v[32:33]
	v_pk_fma_f32 v[92:93], v[38:39], s[22:23], v[90:91] op_sel_hi:[1,0,0]
	v_mul_f32_e32 v13, 0xbf38aa3b, v40
	v_exp_f32_e32 v40, v13
	v_pk_fma_f32 v[92:93], v[38:39], v[92:93], s[24:25] op_sel_hi:[1,1,0]
	v_mul_f32_e32 v13, 0xbf38aa3b, v41
	v_pk_fma_f32 v[92:93], v[38:39], v[92:93], s[34:35] op_sel_hi:[1,1,0]
	v_exp_f32_e32 v41, v13
	v_pk_fma_f32 v[92:93], v[38:39], v[92:93], s[40:41] op_sel_hi:[1,1,0]
	v_and_b32_e32 v37, 0x7fffffff, v33
	v_and_b32_e32 v36, 0x7fffffff, v32
	v_pk_mul_f32 v[38:39], v[38:39], v[92:93]
	v_readlane_b32 s0, v12, 3
	v_max_f32_e32 v32, 0, v32
	v_max_f32_e32 v33, 0, v33
	v_pk_mul_f32 v[36:37], v[36:37], v[38:39]
	v_pk_mul_f32 v[30:31], s[0:1], v[30:31] op_sel_hi:[0,1]
	v_pk_fma_f32 v[32:33], v[40:41], v[36:37], v[32:33] neg_lo:[1,0,0] neg_hi:[1,0,0]
	v_pk_fma_f32 v[30:31], v[30:31], v[238:239], v[242:243]
	v_cvt_pk_f16_f32 v34, v34, v35
	v_cvt_pk_f16_f32 v35, v32, v33
	v_fma_f32 v13, |v30|, s25, 1.0
	ds_write_b64 v137, v[34:35] offset:37888
	v_rcp_f32_e32 v34, v13
	v_fma_f32 v13, |v31|, s25, 1.0
	v_rcp_f32_e32 v35, v13
	v_pk_mul_f32 v[36:37], v[30:31], v[30:31]
	v_pk_mul_f32 v[28:29], s[0:1], v[28:29] op_sel_hi:[0,1]
	v_mul_f32_e32 v13, 0xbf38aa3b, v36
	v_pk_fma_f32 v[38:39], v[34:35], s[22:23], v[90:91] op_sel_hi:[1,0,0]
	v_exp_f32_e32 v36, v13
	v_pk_fma_f32 v[38:39], v[34:35], v[38:39], s[24:25] op_sel_hi:[1,1,0]
	v_mul_f32_e32 v13, 0xbf38aa3b, v37
	v_pk_fma_f32 v[38:39], v[34:35], v[38:39], s[34:35] op_sel_hi:[1,1,0]
	v_pk_fma_f32 v[28:29], v[28:29], v[240:241], v[244:245]
	v_pk_fma_f32 v[38:39], v[34:35], v[38:39], s[40:41] op_sel_hi:[1,1,0]
	v_and_b32_e32 v33, 0x7fffffff, v31
	v_and_b32_e32 v32, 0x7fffffff, v30
	v_exp_f32_e32 v37, v13
	v_pk_mul_f32 v[34:35], v[34:35], v[38:39]
	v_fma_f32 v13, |v28|, s25, 1.0
	v_pk_mul_f32 v[32:33], v[32:33], v[34:35]
	v_rcp_f32_e32 v34, v13
	v_fma_f32 v13, |v29|, s25, 1.0
	v_rcp_f32_e32 v35, v13
	v_max_f32_e32 v30, 0, v30
	v_max_f32_e32 v31, 0, v31
	v_pk_fma_f32 v[30:31], v[36:37], v[32:33], v[30:31] neg_lo:[1,0,0] neg_hi:[1,0,0]
	v_pk_mul_f32 v[36:37], v[28:29], v[28:29]
	v_pk_fma_f32 v[38:39], v[34:35], s[22:23], v[90:91] op_sel_hi:[1,0,0]
	v_mul_f32_e32 v13, 0xbf38aa3b, v36
	v_exp_f32_e32 v36, v13
	v_pk_fma_f32 v[38:39], v[34:35], v[38:39], s[24:25] op_sel_hi:[1,1,0]
	v_mul_f32_e32 v13, 0xbf38aa3b, v37
	v_pk_fma_f32 v[38:39], v[34:35], v[38:39], s[34:35] op_sel_hi:[1,1,0]
	v_exp_f32_e32 v37, v13
	v_pk_fma_f32 v[38:39], v[34:35], v[38:39], s[40:41] op_sel_hi:[1,1,0]
	v_and_b32_e32 v33, 0x7fffffff, v29
	v_and_b32_e32 v32, 0x7fffffff, v28
	v_pk_mul_f32 v[34:35], v[34:35], v[38:39]
	v_readlane_b32 s0, v12, 4
	v_max_f32_e32 v28, 0, v28
	v_max_f32_e32 v29, 0, v29
	v_pk_mul_f32 v[32:33], v[32:33], v[34:35]
	v_pk_mul_f32 v[26:27], s[0:1], v[26:27] op_sel_hi:[0,1]
	v_pk_fma_f32 v[28:29], v[36:37], v[32:33], v[28:29] neg_lo:[1,0,0] neg_hi:[1,0,0]
	v_pk_fma_f32 v[26:27], v[26:27], v[238:239], v[242:243]
	v_cvt_pk_f16_f32 v30, v30, v31
	v_cvt_pk_f16_f32 v31, v28, v29
	v_fma_f32 v13, |v26|, s25, 1.0
	ds_write_b64 v136, v[30:31] offset:38400
	v_rcp_f32_e32 v30, v13
	v_fma_f32 v13, |v27|, s25, 1.0
	v_rcp_f32_e32 v31, v13
	v_pk_mul_f32 v[32:33], v[26:27], v[26:27]
	v_pk_mul_f32 v[24:25], s[0:1], v[24:25] op_sel_hi:[0,1]
	v_mul_f32_e32 v13, 0xbf38aa3b, v32
	v_pk_fma_f32 v[34:35], v[30:31], s[22:23], v[90:91] op_sel_hi:[1,0,0]
	v_exp_f32_e32 v32, v13
	v_pk_fma_f32 v[34:35], v[30:31], v[34:35], s[24:25] op_sel_hi:[1,1,0]
	v_mul_f32_e32 v13, 0xbf38aa3b, v33
	v_pk_fma_f32 v[34:35], v[30:31], v[34:35], s[34:35] op_sel_hi:[1,1,0]
	v_pk_fma_f32 v[24:25], v[24:25], v[240:241], v[244:245]
	v_pk_fma_f32 v[34:35], v[30:31], v[34:35], s[40:41] op_sel_hi:[1,1,0]
	v_and_b32_e32 v29, 0x7fffffff, v27
	v_and_b32_e32 v28, 0x7fffffff, v26
	v_exp_f32_e32 v33, v13
	v_pk_mul_f32 v[30:31], v[30:31], v[34:35]
	v_fma_f32 v13, |v24|, s25, 1.0
	v_pk_mul_f32 v[28:29], v[28:29], v[30:31]
	v_rcp_f32_e32 v30, v13
	v_fma_f32 v13, |v25|, s25, 1.0
	v_rcp_f32_e32 v31, v13
	v_max_f32_e32 v26, 0, v26
	v_max_f32_e32 v27, 0, v27
	v_pk_fma_f32 v[26:27], v[32:33], v[28:29], v[26:27] neg_lo:[1,0,0] neg_hi:[1,0,0]
	v_pk_mul_f32 v[32:33], v[24:25], v[24:25]
	v_pk_fma_f32 v[34:35], v[30:31], s[22:23], v[90:91] op_sel_hi:[1,0,0]
	v_mul_f32_e32 v13, 0xbf38aa3b, v32
	v_exp_f32_e32 v32, v13
	v_pk_fma_f32 v[34:35], v[30:31], v[34:35], s[24:25] op_sel_hi:[1,1,0]
	v_mul_f32_e32 v13, 0xbf38aa3b, v33
	v_pk_fma_f32 v[34:35], v[30:31], v[34:35], s[34:35] op_sel_hi:[1,1,0]
	v_exp_f32_e32 v33, v13
	v_pk_fma_f32 v[34:35], v[30:31], v[34:35], s[40:41] op_sel_hi:[1,1,0]
	v_and_b32_e32 v29, 0x7fffffff, v25
	v_and_b32_e32 v28, 0x7fffffff, v24
	v_pk_mul_f32 v[30:31], v[30:31], v[34:35]
	v_readlane_b32 s0, v12, 5
	v_max_f32_e32 v24, 0, v24
	v_max_f32_e32 v25, 0, v25
	v_pk_mul_f32 v[28:29], v[28:29], v[30:31]
	v_pk_mul_f32 v[22:23], s[0:1], v[22:23] op_sel_hi:[0,1]
	v_pk_fma_f32 v[24:25], v[32:33], v[28:29], v[24:25] neg_lo:[1,0,0] neg_hi:[1,0,0]
	v_pk_fma_f32 v[22:23], v[22:23], v[238:239], v[242:243]
	v_cvt_pk_f16_f32 v26, v26, v27
	v_cvt_pk_f16_f32 v27, v24, v25
	v_fma_f32 v13, |v22|, s25, 1.0
	ds_write_b64 v123, v[26:27] offset:38912
	v_rcp_f32_e32 v26, v13
	v_fma_f32 v13, |v23|, s25, 1.0
	v_rcp_f32_e32 v27, v13
	v_pk_mul_f32 v[28:29], v[22:23], v[22:23]
	v_pk_mul_f32 v[20:21], s[0:1], v[20:21] op_sel_hi:[0,1]
	v_mul_f32_e32 v13, 0xbf38aa3b, v28
	v_pk_fma_f32 v[30:31], v[26:27], s[22:23], v[90:91] op_sel_hi:[1,0,0]
	v_exp_f32_e32 v28, v13
	v_pk_fma_f32 v[30:31], v[26:27], v[30:31], s[24:25] op_sel_hi:[1,1,0]
	v_mul_f32_e32 v13, 0xbf38aa3b, v29
	v_pk_fma_f32 v[30:31], v[26:27], v[30:31], s[34:35] op_sel_hi:[1,1,0]
	v_pk_fma_f32 v[20:21], v[20:21], v[240:241], v[244:245]
	v_pk_fma_f32 v[30:31], v[26:27], v[30:31], s[40:41] op_sel_hi:[1,1,0]
	s_waitcnt vmcnt(7)
	v_add_f32_e32 v92, v170, v171
	v_add_f32_e32 v93, v172, v173
	v_and_b32_e32 v25, 0x7fffffff, v23
	v_and_b32_e32 v24, 0x7fffffff, v22
	v_exp_f32_e32 v29, v13
	v_pk_mul_f32 v[26:27], v[26:27], v[30:31]
	v_fma_f32 v13, |v20|, s25, 1.0
	v_add_f32_e32 v92, v92, v93
	s_waitcnt vmcnt(6)
	v_add_f32_e32 v93, v174, v175
	v_add_f32_e32 v94, v176, v177
	v_pk_mul_f32 v[24:25], v[24:25], v[26:27]
	v_rcp_f32_e32 v26, v13
	v_fma_f32 v13, |v21|, s25, 1.0
	v_add_f32_e32 v93, v93, v94
	s_waitcnt vmcnt(5)
	v_add_f32_e32 v94, v178, v179
	v_add_f32_e32 v95, v180, v181
	v_rcp_f32_e32 v27, v13
	v_add_f32_e32 v94, v94, v95
	s_waitcnt vmcnt(4)
	v_add_f32_e32 v95, v182, v183
	v_add_f32_e32 v96, v184, v185
	v_add_f32_e32 v95, v95, v96
	s_waitcnt vmcnt(3)
	v_add_f32_e32 v96, v186, v187
	v_add_f32_e32 v97, v188, v189
	v_max_f32_e32 v22, 0, v22
	v_max_f32_e32 v23, 0, v23
	v_add_f32_e32 v96, v96, v97
	s_waitcnt vmcnt(2)
	v_add_f32_e32 v97, v190, v191
	v_add_f32_e32 v98, v192, v193
	v_pk_fma_f32 v[22:23], v[28:29], v[24:25], v[22:23] neg_lo:[1,0,0] neg_hi:[1,0,0]
	v_pk_mul_f32 v[28:29], v[20:21], v[20:21]
	v_add_f32_e32 v97, v97, v98
	s_waitcnt vmcnt(1)
	v_add_f32_e32 v98, v194, v195
	v_add_f32_e32 v99, v196, v197
	v_mul_f32_e32 v13, 0xbf38aa3b, v28
	v_pk_fma_f32 v[30:31], v[26:27], s[22:23], v[90:91] op_sel_hi:[1,0,0]
	v_add_f32_e32 v98, v98, v99
	s_waitcnt vmcnt(0)
	v_add_f32_e32 v99, v198, v199
	v_add_f32_e32 v100, v200, v201
	v_exp_f32_e32 v28, v13
	v_pk_fma_f32 v[30:31], v[26:27], v[30:31], s[24:25] op_sel_hi:[1,1,0]
	v_mul_f32_e32 v13, 0xbf38aa3b, v29
	v_add_f32_e32 v99, v99, v100
	v_cndmask_b32_e64 v100, v93, v92, s[4:5]
	v_cndmask_b32_e64 v92, v92, v93, s[4:5]
	v_cndmask_b32_e64 v93, v95, v94, s[4:5]
	v_cndmask_b32_e64 v94, v94, v95, s[4:5]
	v_pk_fma_f32 v[30:31], v[26:27], v[30:31], s[34:35] op_sel_hi:[1,1,0]
	v_exp_f32_e32 v29, v13
	v_add_f32_dpp v93, v93, v94 quad_perm:[1,0,3,2] row_mask:0xf bank_mask:0xf bound_ctrl:1
	v_cndmask_b32_e64 v94, v97, v96, s[4:5]
	v_cndmask_b32_e64 v95, v96, v97, s[4:5]
	v_pk_fma_f32 v[30:31], v[26:27], v[30:31], s[40:41] op_sel_hi:[1,1,0]
	v_cndmask_b32_e64 v96, v98, v99, s[4:5]
	v_add_f32_dpp v94, v94, v95 quad_perm:[1,0,3,2] row_mask:0xf bank_mask:0xf bound_ctrl:1
	v_cndmask_b32_e64 v95, v99, v98, s[4:5]
	v_and_b32_e32 v25, 0x7fffffff, v21
	v_and_b32_e32 v24, 0x7fffffff, v20
	v_pk_mul_f32 v[26:27], v[26:27], v[30:31]
	v_readlane_b32 s0, v12, 6
	v_add_f32_dpp v92, v100, v92 quad_perm:[1,0,3,2] row_mask:0xf bank_mask:0xf bound_ctrl:1
	v_add_f32_dpp v95, v95, v96 quad_perm:[1,0,3,2] row_mask:0xf bank_mask:0xf bound_ctrl:1
	v_max_f32_e32 v20, 0, v20
	v_max_f32_e32 v21, 0, v21
	v_pk_mul_f32 v[24:25], v[24:25], v[26:27]
	v_pk_mul_f32 v[18:19], s[0:1], v[18:19] op_sel_hi:[0,1]
	v_cndmask_b32_e64 v96, v92, v93, s[6:7]
	v_cndmask_b32_e64 v92, v93, v92, s[6:7]
	v_cndmask_b32_e64 v93, v94, v95, s[6:7]
	v_cndmask_b32_e64 v94, v95, v94, s[6:7]
	v_pk_fma_f32 v[20:21], v[28:29], v[24:25], v[20:21] neg_lo:[1,0,0] neg_hi:[1,0,0]
	v_pk_fma_f32 v[18:19], v[18:19], v[238:239], v[242:243]
	v_add_f32_dpp v92, v96, v92 quad_perm:[2,3,0,1] row_mask:0xf bank_mask:0xf bound_ctrl:1
	v_add_f32_dpp v93, v93, v94 quad_perm:[2,3,0,1] row_mask:0xf bank_mask:0xf bound_ctrl:1
	v_cvt_pk_f16_f32 v22, v22, v23
	v_cvt_pk_f16_f32 v23, v20, v21
	v_fma_f32 v13, |v18|, s25, 1.0
	v_cndmask_b32_e64 v94, v92, v93, s[8:9]
	ds_write_b64 v133, v[22:23] offset:39424
	v_rcp_f32_e32 v22, v13
	v_fma_f32 v13, |v19|, s25, 1.0
	v_cndmask_b32_e64 v92, v93, v92, s[8:9]
	v_mov_b32_e32 v93, v94
	v_rcp_f32_e32 v23, v13
	v_pk_mul_f32 v[24:25], v[18:19], v[18:19]
	v_mov_b32_dpp v93, v93 row_shl:4 row_mask:0xf bank_mask:0x5
	v_mul_f32_e32 v13, 0xbf38aa3b, v24
	v_pk_fma_f32 v[26:27], v[22:23], s[22:23], v[90:91] op_sel_hi:[1,0,0]
	v_mov_b32_dpp v93, v94 row_shr:4 row_mask:0xf bank_mask:0xa
	v_add_f32_e32 v92, v92, v93
	v_pk_fma_f32 v[26:27], v[22:23], v[26:27], s[24:25] op_sel_hi:[1,1,0]
	v_pk_mul_f32 v[16:17], s[0:1], v[16:17] op_sel_hi:[0,1]
	v_add_f32_dpp v92, v92, v92 row_ror:8 row_mask:0xf bank_mask:0xf bound_ctrl:1
	v_mov_b32_e32 v93, v92
	s_nop 1
	v_permlane16_swap_b32_e32 v92, v93
	v_pk_fma_f32 v[26:27], v[22:23], v[26:27], s[34:35] op_sel_hi:[1,1,0]
	v_add_f32_e32 v92, v92, v93
	v_exp_f32_e32 v24, v13
	v_pk_fma_f32 v[26:27], v[22:23], v[26:27], s[40:41] op_sel_hi:[1,1,0]
	v_mul_f32_e32 v13, 0xbf38aa3b, v25
	v_pk_fma_f32 v[16:17], v[16:17], v[240:241], v[244:245]
	v_mov_b32_e32 v93, v92
	v_and_b32_e32 v21, 0x7fffffff, v19
	v_and_b32_e32 v20, 0x7fffffff, v18
	v_exp_f32_e32 v25, v13
	v_pk_mul_f32 v[22:23], v[22:23], v[26:27]
	v_fma_f32 v13, |v16|, s25, 1.0
	v_permlane32_swap_b32_e32 v92, v93
	v_pk_mul_f32 v[20:21], v[20:21], v[22:23]
	v_rcp_f32_e32 v22, v13
	v_fma_f32 v13, |v17|, s25, 1.0
	v_add_f32_e32 v92, v92, v93
	v_rcp_f32_e32 v23, v13
	v_mul_f32_e32 v92, 0x3b800000, v92
	v_max_f32_e32 v18, 0, v18
	v_max_f32_e32 v19, 0, v19
	v_readlane_b32 s42, v92, 0
	v_readlane_b32 s44, v92, 1
	v_readlane_b32 s46, v92, 2
	v_readlane_b32 s48, v92, 3
	v_pk_fma_f32 v[18:19], v[24:25], v[20:21], v[18:19] neg_lo:[1,0,0] neg_hi:[1,0,0]
	v_pk_mul_f32 v[24:25], v[16:17], v[16:17]
	v_pk_add_f32 v[160:161], v[172:173], s[42:43] op_sel_hi:[1, 0] neg_lo:[0, 1] neg_hi:[0, 1]
	v_pk_add_f32 v[110:111], v[176:177], s[44:45] op_sel_hi:[1, 0] neg_lo:[0, 1] neg_hi:[0, 1]
	v_pk_add_f32 v[104:105], v[180:181], s[46:47] op_sel_hi:[1, 0] neg_lo:[0, 1] neg_hi:[0, 1]
	v_pk_add_f32 v[100:101], v[184:185], s[48:49] op_sel_hi:[1, 0] neg_lo:[0, 1] neg_hi:[0, 1]
	v_mul_f32_e32 v13, 0xbf38aa3b, v24
	v_pk_add_f32 v[158:159], v[170:171], s[42:43] op_sel_hi:[1, 0] neg_lo:[0, 1] neg_hi:[0, 1]
	v_mul_f32_e32 v78, v161, v161
	v_pk_add_f32 v[162:163], v[174:175], s[44:45] op_sel_hi:[1, 0] neg_lo:[0, 1] neg_hi:[0, 1]
	v_mul_f32_e32 v74, v111, v111
	v_pk_add_f32 v[108:109], v[178:179], s[46:47] op_sel_hi:[1, 0] neg_lo:[0, 1] neg_hi:[0, 1]
	v_mul_f32_e32 v70, v105, v105
	v_pk_add_f32 v[102:103], v[182:183], s[48:49] op_sel_hi:[1, 0] neg_lo:[0, 1] neg_hi:[0, 1]
	v_mul_f32_e32 v66, v101, v101
	v_exp_f32_e32 v24, v13
	v_pk_fma_f32 v[26:27], v[22:23], s[22:23], v[90:91] op_sel_hi:[1,0,0]
	v_mul_f32_e32 v13, 0xbf38aa3b, v25
	v_readlane_b32 s0, v12, 7
	v_fmac_f32_e32 v78, v160, v160
	v_fmac_f32_e32 v74, v110, v110
	v_fmac_f32_e32 v70, v104, v104
	v_fmac_f32_e32 v66, v100, v100
	v_pk_fma_f32 v[26:27], v[22:23], v[26:27], s[24:25] op_sel_hi:[1,1,0]
	v_exp_f32_e32 v25, v13
	v_pk_mul_f32 v[12:13], s[0:1], v[14:15] op_sel_hi:[0,1]
	v_pk_mul_f32 v[10:11], s[0:1], v[10:11] op_sel_hi:[0,1]
	s_movk_i32 s0, 0x6000
	v_fmac_f32_e32 v78, v159, v159
	v_fmac_f32_e32 v74, v163, v163
	v_fmac_f32_e32 v70, v109, v109
	v_fmac_f32_e32 v66, v103, v103
	v_pk_fma_f32 v[26:27], v[22:23], v[26:27], s[34:35] op_sel_hi:[1,1,0]
	v_add_co_u32_e32 v154, vcc, s0, v82
	v_fmac_f32_e32 v78, v158, v158
	v_fmac_f32_e32 v74, v162, v162
	v_fmac_f32_e32 v70, v108, v108
	v_fmac_f32_e32 v66, v102, v102
	v_pk_fma_f32 v[26:27], v[22:23], v[26:27], s[40:41] op_sel_hi:[1,1,0]
	v_addc_co_u32_e32 v155, vcc, 0, v83, vcc
	s_movk_i32 s0, 0x7000
	v_cndmask_b32_e64 v75, v74, v78, s[4:5]
	v_cndmask_b32_e64 v74, v78, v74, s[4:5]
	v_cndmask_b32_e64 v67, v66, v70, s[4:5]
	v_cndmask_b32_e64 v66, v70, v66, s[4:5]
	v_and_b32_e32 v21, 0x7fffffff, v17
	v_and_b32_e32 v20, 0x7fffffff, v16
	v_pk_mul_f32 v[22:23], v[22:23], v[26:27]
	v_add_co_u32_e32 v156, vcc, s0, v82
	v_readlane_b32 s50, v92, 4
	v_readlane_b32 s52, v92, 5
	v_readlane_b32 s54, v92, 6
	v_readlane_b32 s0, v92, 7
	v_add_f32_dpp v74, v75, v74 quad_perm:[1,0,3,2] row_mask:0xf bank_mask:0xf bound_ctrl:1
	v_add_f32_dpp v66, v67, v66 quad_perm:[1,0,3,2] row_mask:0xf bank_mask:0xf bound_ctrl:1
	v_max_f32_e32 v16, 0, v16
	v_max_f32_e32 v17, 0, v17
	v_pk_mul_f32 v[20:21], v[20:21], v[22:23]
	v_cndmask_b32_e64 v67, v74, v66, s[6:7]
	v_cndmask_b32_e64 v66, v66, v74, s[6:7]
	v_pk_add_f32 v[96:97], v[188:189], s[50:51] op_sel_hi:[1, 0] neg_lo:[0, 1] neg_hi:[0, 1]
	v_pk_add_f32 v[92:93], v[192:193], s[52:53] op_sel_hi:[1, 0] neg_lo:[0, 1] neg_hi:[0, 1]
	v_pk_add_f32 v[78:79], v[196:197], s[54:55] op_sel_hi:[1, 0] neg_lo:[0, 1] neg_hi:[0, 1]
	v_pk_add_f32 v[74:75], v[200:201], s[0:1] op_sel_hi:[1, 0] neg_lo:[0, 1] neg_hi:[0, 1]
	v_pk_fma_f32 v[16:17], v[24:25], v[20:21], v[16:17] neg_lo:[1,0,0] neg_hi:[1,0,0]
	v_pk_fma_f32 v[12:13], v[12:13], v[238:239], v[242:243]
	v_pk_add_f32 v[98:99], v[186:187], s[50:51] op_sel_hi:[1, 0] neg_lo:[0, 1] neg_hi:[0, 1]
	v_mul_f32_e32 v62, v97, v97
	v_pk_add_f32 v[94:95], v[190:191], s[52:53] op_sel_hi:[1, 0] neg_lo:[0, 1] neg_hi:[0, 1]
	v_mul_f32_e32 v58, v93, v93
	v_pk_add_f32 v[80:81], v[194:195], s[54:55] op_sel_hi:[1, 0] neg_lo:[0, 1] neg_hi:[0, 1]
	v_mul_f32_e32 v54, v79, v79
	v_pk_add_f32 v[76:77], v[198:199], s[0:1] op_sel_hi:[1, 0] neg_lo:[0, 1] neg_hi:[0, 1]
	v_mul_f32_e32 v50, v75, v75
	v_cvt_pk_f16_f32 v18, v18, v19
	v_cvt_pk_f16_f32 v19, v16, v17
	v_fma_f32 v16, |v12|, s25, 1.0
	v_fma_f32 v17, |v13|, s25, 1.0
	v_fmac_f32_e32 v62, v96, v96
	v_fmac_f32_e32 v58, v92, v92
	v_fmac_f32_e32 v54, v78, v78
	v_fmac_f32_e32 v50, v74, v74
	v_rcp_f32_e32 v16, v16
	v_rcp_f32_e32 v17, v17
	v_fmac_f32_e32 v62, v99, v99
	v_fmac_f32_e32 v58, v95, v95
	v_fmac_f32_e32 v54, v81, v81
	v_fmac_f32_e32 v50, v77, v77
	v_fmac_f32_e32 v62, v98, v98
	v_fmac_f32_e32 v58, v94, v94
	v_fmac_f32_e32 v54, v80, v80
	v_fmac_f32_e32 v50, v76, v76
	v_cndmask_b32_e64 v59, v58, v62, s[4:5]
	v_cndmask_b32_e64 v58, v62, v58, s[4:5]
	v_cndmask_b32_e64 v51, v50, v54, s[4:5]
	v_cndmask_b32_e64 v50, v54, v50, s[4:5]
	v_add_f32_dpp v58, v59, v58 quad_perm:[1,0,3,2] row_mask:0xf bank_mask:0xf bound_ctrl:1
	ds_write_b64 v119, v[18:19] offset:39936
	v_add_f32_dpp v50, v51, v50 quad_perm:[1,0,3,2] row_mask:0xf bank_mask:0xf bound_ctrl:1
	v_pk_mul_f32 v[18:19], v[12:13], v[12:13]
	v_pk_fma_f32 v[20:21], v[16:17], s[22:23], v[90:91] op_sel_hi:[1,0,0]
	v_cndmask_b32_e64 v51, v58, v50, s[6:7]
	v_cndmask_b32_e64 v50, v50, v58, s[6:7]
	v_mul_f32_e32 v18, 0xbf38aa3b, v18
	v_pk_fma_f32 v[20:21], v[16:17], v[20:21], s[24:25] op_sel_hi:[1,1,0]
	v_mul_f32_e32 v19, 0xbf38aa3b, v19
	v_add_f32_dpp v66, v67, v66 quad_perm:[2,3,0,1] row_mask:0xf bank_mask:0xf bound_ctrl:1
	v_add_f32_dpp v50, v51, v50 quad_perm:[2,3,0,1] row_mask:0xf bank_mask:0xf bound_ctrl:1
	v_exp_f32_e32 v18, v18
	v_pk_fma_f32 v[20:21], v[16:17], v[20:21], s[34:35] op_sel_hi:[1,1,0]
	v_exp_f32_e32 v19, v19
	v_cndmask_b32_e64 v51, v66, v50, s[8:9]
	v_pk_fma_f32 v[20:21], v[16:17], v[20:21], s[40:41] op_sel_hi:[1,1,0]
	v_mov_b32_e32 v52, v51
	v_and_b32_e32 v15, 0x7fffffff, v13
	v_and_b32_e32 v14, 0x7fffffff, v12
	v_pk_mul_f32 v[16:17], v[16:17], v[20:21]
	v_mov_b32_dpp v52, v52 row_shl:4 row_mask:0xf bank_mask:0x5
	v_max_f32_e32 v12, 0, v12
	v_max_f32_e32 v13, 0, v13
	v_pk_mul_f32 v[14:15], v[14:15], v[16:17]
	v_cndmask_b32_e64 v50, v50, v66, s[8:9]
	v_mov_b32_dpp v52, v51 row_shr:4 row_mask:0xf bank_mask:0xa
	v_pk_fma_f32 v[12:13], v[18:19], v[14:15], v[12:13] neg_lo:[1,0,0] neg_hi:[1,0,0]
	v_pk_fma_f32 v[10:11], v[10:11], v[240:241], v[244:245]
	v_add_f32_e32 v50, v50, v52
	v_cvt_pk_f16_f32 v12, v12, v13
	v_fma_f32 v13, |v10|, s25, 1.0
	v_add_f32_dpp v50, v50, v50 row_ror:8 row_mask:0xf bank_mask:0xf bound_ctrl:1
	v_rcp_f32_e32 v16, v13
	v_fma_f32 v13, |v11|, s25, 1.0
	v_mov_b32_e32 v51, v50
	v_rcp_f32_e32 v17, v13
	s_nop 0
	v_permlane16_swap_b32_e32 v50, v51
	v_add_f32_e32 v50, v50, v51
	v_mov_b32_e32 v51, v50
	v_pk_mul_f32 v[18:19], v[10:11], v[10:11]
	s_nop 0
	v_permlane32_swap_b32_e32 v50, v51
	v_mul_f32_e32 v13, 0xbf38aa3b, v18
	v_pk_fma_f32 v[20:21], v[16:17], s[22:23], v[90:91] op_sel_hi:[1,0,0]
	v_add_f32_e32 v50, v50, v51
	v_exp_f32_e32 v18, v13
	v_pk_fma_f32 v[20:21], v[16:17], v[20:21], s[24:25] op_sel_hi:[1,1,0]
	v_mul_f32_e32 v13, 0xbf38aa3b, v19
	v_addc_co_u32_e32 v157, vcc, 0, v83, vcc
	v_fmamk_f32 v50, v50, 0x3b800000, v116
	v_pk_fma_f32 v[20:21], v[16:17], v[20:21], s[34:35] op_sel_hi:[1,1,0]
	v_exp_f32_e32 v19, v13
	v_mul_f32_e32 v51, 0x4f800000, v50
	v_cmp_gt_f32_e32 vcc, s35, v50
	v_pk_fma_f32 v[20:21], v[16:17], v[20:21], s[40:41] op_sel_hi:[1,1,0]
	v_and_b32_e32 v15, 0x7fffffff, v11
	v_cndmask_b32_e32 v50, v50, v51, vcc
	v_and_b32_e32 v14, 0x7fffffff, v10
	v_pk_mul_f32 v[16:17], v[16:17], v[20:21]
	v_sqrt_f32_e32 v51, v50
	v_max_f32_e32 v10, 0, v10
	v_max_f32_e32 v11, 0, v11
	v_pk_mul_f32 v[14:15], v[14:15], v[16:17]
	v_add_u32_e32 v52, -1, v51
	v_pk_fma_f32 v[10:11], v[18:19], v[14:15], v[10:11] neg_lo:[1,0,0] neg_hi:[1,0,0]
	v_fma_f32 v53, -v52, v51, v50
	v_cvt_pk_f16_f32 v13, v10, v11
	v_bitop3_b32 v10, v86, s41, v88 bitop3:0x6c
	v_or3_b32 v146, v85, v10, v87
	v_lshlrev_b32_e32 v10, 4, v141
	v_and_or_b32 v147, v10, s41, v84
	v_lshlrev_b32_e32 v10, 4, v142
	v_and_or_b32 v148, v10, s41, v84
	v_lshlrev_b32_e32 v10, 4, v143
	v_cmp_ge_f32_e64 s[0:1], 0, v53
	v_add_u32_e32 v53, 1, v51
	v_and_or_b32 v149, v10, s41, v84
	v_bitop3_b32 v10, v125, v0, 15 bitop3:0x78
	v_cndmask_b32_e64 v52, v51, v52, s[0:1]
	v_fma_f32 v51, -v53, v51, v50
	v_lshl_or_b32 v150, v10, 4, v84
	v_bitop3_b32 v10, v125, v107, 4 bitop3:0x36
	v_cmp_lt_f32_e64 s[0:1], 0, v51
	v_lshl_or_b32 v151, v10, 4, v84
	v_bitop3_b32 v10, v125, v107, 8 bitop3:0x36
	v_cndmask_b32_e64 v51, v52, v53, s[0:1]
	v_lshl_or_b32 v152, v10, 4, v84
	v_bitop3_b32 v10, v125, v107, 12 bitop3:0x36
	v_mul_f32_e32 v52, 0x37800000, v51
	ds_write_b64 v146, v[12:13] offset:40448
	v_lshl_or_b32 v153, v10, 4, v84
	v_cndmask_b32_e32 v51, v51, v52, vcc
	v_cmp_class_f32_e32 vcc, v50, v117
	ds_read_b128 v[38:41], v115 offset:32768
	ds_read_b128 v[34:37], v147 offset:32768
	ds_read_b128 v[30:33], v148 offset:32768
	ds_read_b128 v[26:29], v149 offset:32768
	ds_read_b128 v[22:25], v150 offset:33024
	ds_read_b128 v[18:21], v151 offset:33024
	ds_read_b128 v[14:17], v152 offset:33024
	ds_read_b128 v[10:13], v153 offset:33024
	s_movk_i32 s57, 0x7000
	s_nop 1
	v_add_co_u32_e64 v236, s[60:61], s57, v82
	s_nop 1
	v_addc_co_u32_e64 v237, s[60:61], 0, v83, s[60:61]
	s_nop 1
	global_load_dwordx4 v[206:209], v[236:237], off offset:-3072 nt
	global_load_dwordx4 v[210:213], v[236:237], off offset:-2048 nt
	global_load_dwordx4 v[214:217], v[236:237], off offset:-1024 nt
	global_load_dwordx4 v[202:205], v[236:237], off offset:-4096 nt
	global_load_dwordx4 v[218:221], v[236:237], off nt
	v_cndmask_b32_e32 v154, v51, v50, vcc
	v_div_scale_f32 v155, s[0:1], v154, v154, 1.0
	v_rcp_f32_e32 v164, v155
	global_load_dwordx4 v[222:225], v[236:237], off offset:1024 nt
	global_load_dwordx4 v[226:229], v[236:237], off offset:2048 nt
	global_load_dwordx4 v[230:233], v[236:237], off offset:3072 nt
	v_fma_f32 v156, -v155, v164, 1.0
	v_fmac_f32_e32 v164, v156, v164
	v_div_scale_f32 v156, vcc, 1.0, v154, 1.0
	v_mul_f32_e32 v157, v156, v164
	v_fma_f32 v165, -v155, v157, v156
	v_fmac_f32_e32 v157, v165, v164
	v_fma_f32 v155, -v155, v157, v156
	v_div_fmas_f32 v155, v155, v164, v157
	v_div_fixup_f32 v154, v155, v154, 1.0
	s_nop 0
	v_readlane_b32 s0, v154, 0
	s_nop 1
	v_pk_mul_f32 v[156:157], s[0:1], v[158:159] op_sel_hi:[0,1]
	v_pk_fma_f32 v[156:157], v[156:157], v[238:239], v[242:243]
	s_nop 0
	v_fma_f32 v155, |v156|, s25, 1.0
	v_rcp_f32_e32 v164, v155
	v_fma_f32 v155, |v157|, s25, 1.0
	v_rcp_f32_e32 v165, v155
	v_pk_mul_f32 v[166:167], v[156:157], v[156:157]
	v_and_b32_e32 v159, 0x7fffffff, v157
	v_mul_f32_e32 v155, 0xbf38aa3b, v166
	v_pk_fma_f32 v[168:169], v[164:165], s[22:23], v[90:91] op_sel_hi:[1,0,0]
	v_exp_f32_e32 v166, v155
	v_pk_fma_f32 v[168:169], v[164:165], v[168:169], s[24:25] op_sel_hi:[1,1,0]
	v_mul_f32_e32 v155, 0xbf38aa3b, v167
	v_pk_fma_f32 v[168:169], v[164:165], v[168:169], s[34:35] op_sel_hi:[1,1,0]
	v_exp_f32_e32 v167, v155
	v_pk_fma_f32 v[168:169], v[164:165], v[168:169], s[40:41] op_sel_hi:[1,1,0]
	v_and_b32_e32 v158, 0x7fffffff, v156
	v_pk_mul_f32 v[164:165], v[164:165], v[168:169]
	v_max_f32_e32 v156, 0, v156
	v_max_f32_e32 v157, 0, v157
	v_pk_mul_f32 v[158:159], v[158:159], v[164:165]
	s_nop 0
	v_pk_fma_f32 v[156:157], v[166:167], v[158:159], v[156:157] neg_lo:[1,0,0] neg_hi:[1,0,0]
	v_pk_mul_f32 v[158:159], s[0:1], v[160:161] op_sel_hi:[0,1]
	v_pk_fma_f32 v[158:159], v[158:159], v[240:241], v[244:245]
	v_cvt_pk_f16_f32 v156, v156, v157
	v_fma_f32 v155, |v158|, s25, 1.0
	v_rcp_f32_e32 v164, v155
	v_fma_f32 v155, |v159|, s25, 1.0
	v_rcp_f32_e32 v165, v155
	v_pk_mul_f32 v[166:167], v[158:159], v[158:159]
	v_and_b32_e32 v161, 0x7fffffff, v159
	v_mul_f32_e32 v155, 0xbf38aa3b, v166
	v_pk_fma_f32 v[168:169], v[164:165], s[22:23], v[90:91] op_sel_hi:[1,0,0]
	v_exp_f32_e32 v166, v155
	v_pk_fma_f32 v[168:169], v[164:165], v[168:169], s[24:25] op_sel_hi:[1,1,0]
	v_mul_f32_e32 v155, 0xbf38aa3b, v167
	v_pk_fma_f32 v[168:169], v[164:165], v[168:169], s[34:35] op_sel_hi:[1,1,0]
	v_exp_f32_e32 v167, v155
	v_pk_fma_f32 v[168:169], v[164:165], v[168:169], s[40:41] op_sel_hi:[1,1,0]
	v_and_b32_e32 v160, 0x7fffffff, v158
	v_pk_mul_f32 v[164:165], v[164:165], v[168:169]
	v_max_f32_e32 v158, 0, v158
	v_max_f32_e32 v159, 0, v159
	v_pk_mul_f32 v[160:161], v[160:161], v[164:165]
	v_readlane_b32 s0, v154, 1
	v_pk_fma_f32 v[158:159], v[166:167], v[160:161], v[158:159] neg_lo:[1,0,0] neg_hi:[1,0,0]
	s_nop 0
	v_cvt_pk_f16_f32 v157, v158, v159
	ds_write_b64 v140, v[156:157] offset:32768
	v_pk_mul_f32 v[156:157], s[0:1], v[162:163] op_sel_hi:[0,1]
	v_pk_fma_f32 v[156:157], v[156:157], v[238:239], v[242:243]
	v_pk_mul_f32 v[110:111], s[0:1], v[110:111] op_sel_hi:[0,1]
	v_fma_f32 v140, |v156|, s25, 1.0
	v_rcp_f32_e32 v160, v140
	v_fma_f32 v140, |v157|, s25, 1.0
	v_rcp_f32_e32 v161, v140
	v_pk_mul_f32 v[162:163], v[156:157], v[156:157]
	v_pk_fma_f32 v[110:111], v[110:111], v[240:241], v[244:245]
	v_mul_f32_e32 v140, 0xbf38aa3b, v162
	v_pk_fma_f32 v[164:165], v[160:161], s[22:23], v[90:91] op_sel_hi:[1,0,0]
	v_exp_f32_e32 v162, v140
	v_pk_fma_f32 v[164:165], v[160:161], v[164:165], s[24:25] op_sel_hi:[1,1,0]
	v_mul_f32_e32 v140, 0xbf38aa3b, v163
	v_pk_fma_f32 v[164:165], v[160:161], v[164:165], s[34:35] op_sel_hi:[1,1,0]
	v_and_b32_e32 v159, 0x7fffffff, v157
	v_pk_fma_f32 v[164:165], v[160:161], v[164:165], s[40:41] op_sel_hi:[1,1,0]
	v_and_b32_e32 v158, 0x7fffffff, v156
	v_exp_f32_e32 v163, v140
	v_pk_mul_f32 v[160:161], v[160:161], v[164:165]
	v_fma_f32 v140, |v110|, s25, 1.0
	v_pk_mul_f32 v[158:159], v[158:159], v[160:161]
	v_rcp_f32_e32 v160, v140
	v_fma_f32 v140, |v111|, s25, 1.0
	v_rcp_f32_e32 v161, v140
	v_max_f32_e32 v156, 0, v156
	v_max_f32_e32 v157, 0, v157
	v_pk_fma_f32 v[156:157], v[162:163], v[158:159], v[156:157] neg_lo:[1,0,0] neg_hi:[1,0,0]
	v_pk_mul_f32 v[162:163], v[110:111], v[110:111]
	v_pk_fma_f32 v[164:165], v[160:161], s[22:23], v[90:91] op_sel_hi:[1,0,0]
	v_mul_f32_e32 v140, 0xbf38aa3b, v162
	v_exp_f32_e32 v162, v140
	v_pk_fma_f32 v[164:165], v[160:161], v[164:165], s[24:25] op_sel_hi:[1,1,0]
	v_mul_f32_e32 v140, 0xbf38aa3b, v163
	v_pk_fma_f32 v[164:165], v[160:161], v[164:165], s[34:35] op_sel_hi:[1,1,0]
	v_exp_f32_e32 v163, v140
	v_pk_fma_f32 v[164:165], v[160:161], v[164:165], s[40:41] op_sel_hi:[1,1,0]
	v_and_b32_e32 v159, 0x7fffffff, v111
	v_and_b32_e32 v158, 0x7fffffff, v110
	v_pk_mul_f32 v[160:161], v[160:161], v[164:165]
	v_max_f32_e32 v110, 0, v110
	v_max_f32_e32 v111, 0, v111
	v_pk_mul_f32 v[158:159], v[158:159], v[160:161]
	v_readlane_b32 s0, v154, 2
	v_pk_fma_f32 v[110:111], v[162:163], v[158:159], v[110:111] neg_lo:[1,0,0] neg_hi:[1,0,0]
	v_cvt_pk_f16_f32 v156, v156, v157
	v_pk_mul_f32 v[108:109], s[0:1], v[108:109] op_sel_hi:[0,1]
	v_cvt_pk_f16_f32 v157, v110, v111
	v_pk_fma_f32 v[108:109], v[108:109], v[238:239], v[242:243]
	ds_write_b64 v138, v[156:157] offset:33280
	v_fma_f32 v138, |v108|, s25, 1.0
	v_rcp_f32_e32 v156, v138
	v_fma_f32 v138, |v109|, s25, 1.0
	v_rcp_f32_e32 v157, v138
	v_pk_mul_f32 v[158:159], v[108:109], v[108:109]
	v_and_b32_e32 v111, 0x7fffffff, v109
	v_mul_f32_e32 v138, 0xbf38aa3b, v158
	v_pk_fma_f32 v[160:161], v[156:157], s[22:23], v[90:91] op_sel_hi:[1,0,0]
	v_exp_f32_e32 v158, v138
	v_pk_fma_f32 v[160:161], v[156:157], v[160:161], s[24:25] op_sel_hi:[1,1,0]
	v_mul_f32_e32 v138, 0xbf38aa3b, v159
	v_pk_fma_f32 v[160:161], v[156:157], v[160:161], s[34:35] op_sel_hi:[1,1,0]
	v_exp_f32_e32 v159, v138
	v_pk_fma_f32 v[160:161], v[156:157], v[160:161], s[40:41] op_sel_hi:[1,1,0]
	v_and_b32_e32 v110, 0x7fffffff, v108
	v_pk_mul_f32 v[156:157], v[156:157], v[160:161]
	v_max_f32_e32 v108, 0, v108
	v_max_f32_e32 v109, 0, v109
	v_pk_mul_f32 v[110:111], v[110:111], v[156:157]
	v_pk_mul_f32 v[104:105], s[0:1], v[104:105] op_sel_hi:[0,1]
	v_pk_fma_f32 v[108:109], v[158:159], v[110:111], v[108:109] neg_lo:[1,0,0] neg_hi:[1,0,0]
	v_pk_fma_f32 v[104:105], v[104:105], v[240:241], v[244:245]
	v_cvt_pk_f16_f32 v108, v108, v109
	v_fma_f32 v109, |v104|, s25, 1.0
	v_rcp_f32_e32 v156, v109
	v_fma_f32 v109, |v105|, s25, 1.0
	v_rcp_f32_e32 v157, v109
	v_pk_mul_f32 v[158:159], v[104:105], v[104:105]
	v_and_b32_e32 v111, 0x7fffffff, v105
	v_mul_f32_e32 v109, 0xbf38aa3b, v158
	v_pk_fma_f32 v[160:161], v[156:157], s[22:23], v[90:91] op_sel_hi:[1,0,0]
	v_exp_f32_e32 v158, v109
	v_pk_fma_f32 v[160:161], v[156:157], v[160:161], s[24:25] op_sel_hi:[1,1,0]
	v_mul_f32_e32 v109, 0xbf38aa3b, v159
	v_pk_fma_f32 v[160:161], v[156:157], v[160:161], s[34:35] op_sel_hi:[1,1,0]
	v_exp_f32_e32 v159, v109
	v_pk_fma_f32 v[160:161], v[156:157], v[160:161], s[40:41] op_sel_hi:[1,1,0]
	v_and_b32_e32 v110, 0x7fffffff, v104
	v_pk_mul_f32 v[156:157], v[156:157], v[160:161]
	v_max_f32_e32 v104, 0, v104
	v_max_f32_e32 v105, 0, v105
	v_pk_mul_f32 v[110:111], v[110:111], v[156:157]
	v_readlane_b32 s0, v154, 3
	v_pk_fma_f32 v[104:105], v[158:159], v[110:111], v[104:105] neg_lo:[1,0,0] neg_hi:[1,0,0]
	s_nop 0
	v_pk_mul_f32 v[102:103], s[0:1], v[102:103] op_sel_hi:[0,1]
	v_cvt_pk_f16_f32 v109, v104, v105
	v_pk_fma_f32 v[102:103], v[102:103], v[238:239], v[242:243]
	ds_write_b64 v135, v[108:109] offset:33792
	v_fma_f32 v108, |v102|, s25, 1.0
	v_fma_f32 v109, |v103|, s25, 1.0
	v_rcp_f32_e32 v108, v108
	v_rcp_f32_e32 v109, v109
	v_pk_mul_f32 v[110:111], v[102:103], v[102:103]
	v_and_b32_e32 v105, 0x7fffffff, v103
	v_mul_f32_e32 v110, 0xbf38aa3b, v110
	v_pk_fma_f32 v[156:157], v[108:109], s[22:23], v[90:91] op_sel_hi:[1,0,0]
	v_mul_f32_e32 v111, 0xbf38aa3b, v111
	v_pk_fma_f32 v[156:157], v[108:109], v[156:157], s[24:25] op_sel_hi:[1,1,0]
	v_exp_f32_e32 v110, v110
	v_pk_fma_f32 v[156:157], v[108:109], v[156:157], s[34:35] op_sel_hi:[1,1,0]
	v_exp_f32_e32 v111, v111
	v_pk_fma_f32 v[156:157], v[108:109], v[156:157], s[40:41] op_sel_hi:[1,1,0]
	v_and_b32_e32 v104, 0x7fffffff, v102
	v_pk_mul_f32 v[108:109], v[108:109], v[156:157]
	v_max_f32_e32 v102, 0, v102
	v_max_f32_e32 v103, 0, v103
	v_pk_mul_f32 v[104:105], v[104:105], v[108:109]
	v_pk_mul_f32 v[100:101], s[0:1], v[100:101] op_sel_hi:[0,1]
	v_pk_fma_f32 v[102:103], v[110:111], v[104:105], v[102:103] neg_lo:[1,0,0] neg_hi:[1,0,0]
	v_pk_fma_f32 v[100:101], v[100:101], v[240:241], v[244:245]
	v_cvt_pk_f16_f32 v102, v102, v103
	v_fma_f32 v103, |v100|, s25, 1.0
	v_rcp_f32_e32 v108, v103
	v_fma_f32 v103, |v101|, s25, 1.0
	v_rcp_f32_e32 v109, v103
	v_pk_mul_f32 v[110:111], v[100:101], v[100:101]
	v_and_b32_e32 v105, 0x7fffffff, v101
	v_mul_f32_e32 v103, 0xbf38aa3b, v110
	v_pk_fma_f32 v[156:157], v[108:109], s[22:23], v[90:91] op_sel_hi:[1,0,0]
	v_exp_f32_e32 v110, v103
	v_pk_fma_f32 v[156:157], v[108:109], v[156:157], s[24:25] op_sel_hi:[1,1,0]
	v_mul_f32_e32 v103, 0xbf38aa3b, v111
	v_pk_fma_f32 v[156:157], v[108:109], v[156:157], s[34:35] op_sel_hi:[1,1,0]
	v_exp_f32_e32 v111, v103
	v_pk_fma_f32 v[156:157], v[108:109], v[156:157], s[40:41] op_sel_hi:[1,1,0]
	v_and_b32_e32 v104, 0x7fffffff, v100
	v_pk_mul_f32 v[108:109], v[108:109], v[156:157]
	v_max_f32_e32 v100, 0, v100
	v_max_f32_e32 v101, 0, v101
	v_pk_mul_f32 v[104:105], v[104:105], v[108:109]
	v_readlane_b32 s0, v154, 4
	v_pk_fma_f32 v[100:101], v[110:111], v[104:105], v[100:101] neg_lo:[1,0,0] neg_hi:[1,0,0]
	s_nop 0
	v_pk_mul_f32 v[98:99], s[0:1], v[98:99] op_sel_hi:[0,1]
	v_cvt_pk_f16_f32 v103, v100, v101
	v_pk_fma_f32 v[98:99], v[98:99], v[238:239], v[242:243]
	ds_write_b64 v134, v[102:103] offset:34304
	v_fma_f32 v102, |v98|, s25, 1.0
	v_fma_f32 v103, |v99|, s25, 1.0
	v_rcp_f32_e32 v102, v102
	v_rcp_f32_e32 v103, v103
	v_pk_mul_f32 v[104:105], v[98:99], v[98:99]
	v_and_b32_e32 v101, 0x7fffffff, v99
	v_mul_f32_e32 v104, 0xbf38aa3b, v104
	v_pk_fma_f32 v[108:109], v[102:103], s[22:23], v[90:91] op_sel_hi:[1,0,0]
	v_mul_f32_e32 v105, 0xbf38aa3b, v105
	v_pk_fma_f32 v[108:109], v[102:103], v[108:109], s[24:25] op_sel_hi:[1,1,0]
	v_exp_f32_e32 v104, v104
	v_pk_fma_f32 v[108:109], v[102:103], v[108:109], s[34:35] op_sel_hi:[1,1,0]
	v_exp_f32_e32 v105, v105
	v_pk_fma_f32 v[108:109], v[102:103], v[108:109], s[40:41] op_sel_hi:[1,1,0]
	v_and_b32_e32 v100, 0x7fffffff, v98
	v_pk_mul_f32 v[102:103], v[102:103], v[108:109]
	v_max_f32_e32 v98, 0, v98
	v_max_f32_e32 v99, 0, v99
	v_pk_mul_f32 v[100:101], v[100:101], v[102:103]
	v_pk_mul_f32 v[96:97], s[0:1], v[96:97] op_sel_hi:[0,1]
	v_pk_fma_f32 v[98:99], v[104:105], v[100:101], v[98:99] neg_lo:[1,0,0] neg_hi:[1,0,0]
	v_pk_fma_f32 v[96:97], v[96:97], v[240:241], v[244:245]
	v_cvt_pk_f16_f32 v98, v98, v99
	v_fma_f32 v99, |v96|, s25, 1.0
	v_rcp_f32_e32 v102, v99
	v_fma_f32 v99, |v97|, s25, 1.0
	v_rcp_f32_e32 v103, v99
	v_pk_mul_f32 v[104:105], v[96:97], v[96:97]
	v_and_b32_e32 v101, 0x7fffffff, v97
	v_mul_f32_e32 v99, 0xbf38aa3b, v104
	v_pk_fma_f32 v[108:109], v[102:103], s[22:23], v[90:91] op_sel_hi:[1,0,0]
	v_exp_f32_e32 v104, v99
	v_pk_fma_f32 v[108:109], v[102:103], v[108:109], s[24:25] op_sel_hi:[1,1,0]
	v_mul_f32_e32 v99, 0xbf38aa3b, v105
	v_pk_fma_f32 v[108:109], v[102:103], v[108:109], s[34:35] op_sel_hi:[1,1,0]
	v_exp_f32_e32 v105, v99
	v_pk_fma_f32 v[108:109], v[102:103], v[108:109], s[40:41] op_sel_hi:[1,1,0]
	v_and_b32_e32 v100, 0x7fffffff, v96
	v_pk_mul_f32 v[102:103], v[102:103], v[108:109]
	v_max_f32_e32 v96, 0, v96
	v_max_f32_e32 v97, 0, v97
	v_pk_mul_f32 v[100:101], v[100:101], v[102:103]
	v_readlane_b32 s0, v154, 5
	v_pk_fma_f32 v[96:97], v[104:105], v[100:101], v[96:97] neg_lo:[1,0,0] neg_hi:[1,0,0]
	v_mov_b32_e32 v104, 0
	v_pk_mul_f32 v[94:95], s[0:1], v[94:95] op_sel_hi:[0,1]
	v_cvt_pk_f16_f32 v99, v96, v97
	v_pk_fma_f32 v[94:95], v[94:95], v[238:239], v[242:243]
	ds_write_b64 v120, v[98:99] offset:34816
	v_fma_f32 v98, |v94|, s25, 1.0
	v_fma_f32 v99, |v95|, s25, 1.0
	v_rcp_f32_e32 v98, v98
	v_rcp_f32_e32 v99, v99
	v_pk_mul_f32 v[100:101], v[94:95], v[94:95]
	v_and_b32_e32 v97, 0x7fffffff, v95
	v_mul_f32_e32 v100, 0xbf38aa3b, v100
	v_pk_fma_f32 v[102:103], v[98:99], s[22:23], v[90:91] op_sel_hi:[1,0,0]
	v_mul_f32_e32 v101, 0xbf38aa3b, v101
	v_pk_fma_f32 v[102:103], v[98:99], v[102:103], s[24:25] op_sel_hi:[1,1,0]
	v_exp_f32_e32 v100, v100
	v_pk_fma_f32 v[102:103], v[98:99], v[102:103], s[34:35] op_sel_hi:[1,1,0]
	v_exp_f32_e32 v101, v101
	v_pk_fma_f32 v[102:103], v[98:99], v[102:103], s[40:41] op_sel_hi:[1,1,0]
	v_and_b32_e32 v96, 0x7fffffff, v94
	v_pk_mul_f32 v[98:99], v[98:99], v[102:103]
	v_max_f32_e32 v94, 0, v94
	v_max_f32_e32 v95, 0, v95
	v_pk_mul_f32 v[96:97], v[96:97], v[98:99]
	v_pk_mul_f32 v[92:93], s[0:1], v[92:93] op_sel_hi:[0,1]
	v_pk_fma_f32 v[94:95], v[100:101], v[96:97], v[94:95] neg_lo:[1,0,0] neg_hi:[1,0,0]
	v_pk_fma_f32 v[92:93], v[92:93], v[240:241], v[244:245]
	v_cvt_pk_f16_f32 v94, v94, v95
	v_fma_f32 v95, |v92|, s25, 1.0
	v_rcp_f32_e32 v98, v95
	v_fma_f32 v95, |v93|, s25, 1.0
	v_rcp_f32_e32 v99, v95
	v_pk_mul_f32 v[100:101], v[92:93], v[92:93]
	v_and_b32_e32 v97, 0x7fffffff, v93
	v_mul_f32_e32 v95, 0xbf38aa3b, v100
	v_pk_fma_f32 v[102:103], v[98:99], s[22:23], v[90:91] op_sel_hi:[1,0,0]
	v_exp_f32_e32 v100, v95
	v_pk_fma_f32 v[102:103], v[98:99], v[102:103], s[24:25] op_sel_hi:[1,1,0]
	v_mul_f32_e32 v95, 0xbf38aa3b, v101
	v_pk_fma_f32 v[102:103], v[98:99], v[102:103], s[34:35] op_sel_hi:[1,1,0]
	v_exp_f32_e32 v101, v95
	v_pk_fma_f32 v[102:103], v[98:99], v[102:103], s[40:41] op_sel_hi:[1,1,0]
	v_and_b32_e32 v96, 0x7fffffff, v92
	v_pk_mul_f32 v[98:99], v[98:99], v[102:103]
	v_max_f32_e32 v92, 0, v92
	v_max_f32_e32 v93, 0, v93
	v_pk_mul_f32 v[96:97], v[96:97], v[98:99]
	v_readlane_b32 s0, v154, 6
	v_pk_fma_f32 v[92:93], v[100:101], v[96:97], v[92:93] neg_lo:[1,0,0] neg_hi:[1,0,0]
	s_waitcnt vmcnt(1)
	v_add_f32_e32 v100, v228, v229
	v_pk_mul_f32 v[80:81], s[0:1], v[80:81] op_sel_hi:[0,1]
	v_cvt_pk_f16_f32 v95, v92, v93
	v_pk_fma_f32 v[80:81], v[80:81], v[238:239], v[242:243]
	ds_write_b64 v121, v[94:95] offset:35328
	v_fma_f32 v94, |v80|, s25, 1.0
	v_fma_f32 v95, |v81|, s25, 1.0
	v_rcp_f32_e32 v94, v94
	v_rcp_f32_e32 v95, v95
	v_pk_mul_f32 v[96:97], v[80:81], v[80:81]
	v_and_b32_e32 v93, 0x7fffffff, v81
	v_mul_f32_e32 v96, 0xbf38aa3b, v96
	v_pk_fma_f32 v[98:99], v[94:95], s[22:23], v[90:91] op_sel_hi:[1,0,0]
	v_mul_f32_e32 v97, 0xbf38aa3b, v97
	v_pk_fma_f32 v[98:99], v[94:95], v[98:99], s[24:25] op_sel_hi:[1,1,0]
	v_exp_f32_e32 v96, v96
	v_pk_fma_f32 v[98:99], v[94:95], v[98:99], s[34:35] op_sel_hi:[1,1,0]
	v_exp_f32_e32 v97, v97
	v_pk_fma_f32 v[98:99], v[94:95], v[98:99], s[40:41] op_sel_hi:[1,1,0]
	v_and_b32_e32 v92, 0x7fffffff, v80
	v_pk_mul_f32 v[94:95], v[94:95], v[98:99]
	v_max_f32_e32 v80, 0, v80
	v_max_f32_e32 v81, 0, v81
	v_pk_mul_f32 v[92:93], v[92:93], v[94:95]
	v_pk_mul_f32 v[78:79], s[0:1], v[78:79] op_sel_hi:[0,1]
	v_pk_fma_f32 v[80:81], v[96:97], v[92:93], v[80:81] neg_lo:[1,0,0] neg_hi:[1,0,0]
	v_pk_fma_f32 v[78:79], v[78:79], v[240:241], v[244:245]
	v_cvt_pk_f16_f32 v80, v80, v81
	v_fma_f32 v81, |v78|, s25, 1.0
	v_rcp_f32_e32 v94, v81
	v_fma_f32 v81, |v79|, s25, 1.0
	v_rcp_f32_e32 v95, v81
	v_pk_mul_f32 v[96:97], v[78:79], v[78:79]
	v_and_b32_e32 v93, 0x7fffffff, v79
	v_mul_f32_e32 v81, 0xbf38aa3b, v96
	v_pk_fma_f32 v[98:99], v[94:95], s[22:23], v[90:91] op_sel_hi:[1,0,0]
	v_exp_f32_e32 v96, v81
	v_pk_fma_f32 v[98:99], v[94:95], v[98:99], s[24:25] op_sel_hi:[1,1,0]
	v_mul_f32_e32 v81, 0xbf38aa3b, v97
	v_pk_fma_f32 v[98:99], v[94:95], v[98:99], s[34:35] op_sel_hi:[1,1,0]
	v_exp_f32_e32 v97, v81
	v_pk_fma_f32 v[98:99], v[94:95], v[98:99], s[40:41] op_sel_hi:[1,1,0]
	v_and_b32_e32 v92, 0x7fffffff, v78
	v_pk_mul_f32 v[94:95], v[94:95], v[98:99]
	v_max_f32_e32 v78, 0, v78
	v_max_f32_e32 v79, 0, v79
	v_pk_mul_f32 v[92:93], v[92:93], v[94:95]
	v_readlane_b32 s0, v154, 7
	v_pk_fma_f32 v[78:79], v[96:97], v[92:93], v[78:79] neg_lo:[1,0,0] neg_hi:[1,0,0]
	v_add_f32_e32 v97, v224, v225
	v_pk_mul_f32 v[76:77], s[0:1], v[76:77] op_sel_hi:[0,1]
	v_cvt_pk_f16_f32 v81, v78, v79
	v_pk_fma_f32 v[76:77], v[76:77], v[238:239], v[242:243]
	ds_write_b64 v118, v[80:81] offset:35840
	v_fma_f32 v80, |v76|, s25, 1.0
	v_fma_f32 v81, |v77|, s25, 1.0
	v_rcp_f32_e32 v80, v80
	v_rcp_f32_e32 v81, v81
	v_pk_mul_f32 v[92:93], v[76:77], v[76:77]
	v_and_b32_e32 v79, 0x7fffffff, v77
	v_mul_f32_e32 v92, 0xbf38aa3b, v92
	v_pk_fma_f32 v[94:95], v[80:81], s[22:23], v[90:91] op_sel_hi:[1,0,0]
	v_mul_f32_e32 v93, 0xbf38aa3b, v93
	v_pk_fma_f32 v[94:95], v[80:81], v[94:95], s[24:25] op_sel_hi:[1,1,0]
	v_exp_f32_e32 v92, v92
	v_pk_fma_f32 v[94:95], v[80:81], v[94:95], s[34:35] op_sel_hi:[1,1,0]
	v_exp_f32_e32 v93, v93
	v_pk_fma_f32 v[94:95], v[80:81], v[94:95], s[40:41] op_sel_hi:[1,1,0]
	v_and_b32_e32 v78, 0x7fffffff, v76
	v_pk_mul_f32 v[80:81], v[80:81], v[94:95]
	v_max_f32_e32 v76, 0, v76
	v_max_f32_e32 v77, 0, v77
	v_pk_mul_f32 v[78:79], v[78:79], v[80:81]
	v_pk_mul_f32 v[74:75], s[0:1], v[74:75] op_sel_hi:[0,1]
	v_pk_fma_f32 v[76:77], v[92:93], v[78:79], v[76:77] neg_lo:[1,0,0] neg_hi:[1,0,0]
	v_pk_fma_f32 v[92:93], v[74:75], v[240:241], v[244:245]
	v_cvt_pk_f16_f32 v80, v76, v77
	v_fma_f32 v74, |v92|, s25, 1.0
	v_fma_f32 v75, |v93|, s25, 1.0
	v_rcp_f32_e32 v74, v74
	v_rcp_f32_e32 v75, v75
	v_pk_mul_f32 v[76:77], v[92:93], v[92:93]
	s_waitcnt vmcnt(0)
	v_add_f32_e32 v101, v232, v233
	v_mul_f32_e32 v76, 0xbf38aa3b, v76
	v_pk_fma_f32 v[78:79], v[74:75], s[22:23], v[90:91] op_sel_hi:[1,0,0]
	v_exp_f32_e32 v96, v76
	v_pk_fma_f32 v[78:79], v[74:75], v[78:79], s[24:25] op_sel_hi:[1,1,0]
	v_add_f32_e32 v76, v208, v209
	v_pk_fma_f32 v[78:79], v[74:75], v[78:79], s[34:35] op_sel_hi:[1,1,0]
	v_mul_f32_e32 v81, 0xbf38aa3b, v77
	v_pk_fma_f32 v[78:79], v[74:75], v[78:79], s[40:41] op_sel_hi:[1,1,0]
	v_add_f32_e32 v77, v212, v213
	v_pk_mul_f32 v[98:99], v[74:75], v[78:79]
	v_add_f32_e32 v74, v202, v203
	v_add_f32_e32 v75, v204, v205
	v_add_f32_e32 v74, v74, v75
	v_add_f32_e32 v75, v206, v207
	v_add_f32_e32 v75, v75, v76
	v_add_f32_e32 v76, v210, v211
	v_add_f32_e32 v76, v76, v77
	v_add_f32_e32 v77, v214, v215
	v_add_f32_e32 v78, v216, v217
	v_add_f32_e32 v77, v77, v78
	v_add_f32_e32 v78, v218, v219
	v_add_f32_e32 v79, v220, v221
	v_add_f32_e32 v78, v78, v79
	v_add_f32_e32 v79, v222, v223
	v_add_f32_e32 v79, v79, v97
	v_add_f32_e32 v97, v226, v227
	v_add_f32_e32 v97, v97, v100
	v_add_f32_e32 v100, v230, v231
	v_add_f32_e32 v100, v100, v101
	v_cndmask_b32_e64 v101, v75, v74, s[4:5]
	v_cndmask_b32_e64 v74, v74, v75, s[4:5]
	v_cndmask_b32_e64 v75, v77, v76, s[4:5]
	v_cndmask_b32_e64 v76, v76, v77, s[4:5]
	v_cndmask_b32_e64 v77, v78, v79, s[4:5]
	v_add_f32_dpp v74, v101, v74 quad_perm:[1,0,3,2] row_mask:0xf bank_mask:0xf bound_ctrl:1
	v_add_f32_dpp v75, v75, v76 quad_perm:[1,0,3,2] row_mask:0xf bank_mask:0xf bound_ctrl:1
	v_cndmask_b32_e64 v76, v79, v78, s[4:5]
	v_cndmask_b32_e64 v78, v97, v100, s[4:5]
	v_and_b32_e32 v95, 0x7fffffff, v93
	v_add_f32_dpp v76, v76, v77 quad_perm:[1,0,3,2] row_mask:0xf bank_mask:0xf bound_ctrl:1
	v_cndmask_b32_e64 v77, v100, v97, s[4:5]
	v_exp_f32_e32 v97, v81
	v_and_b32_e32 v94, 0x7fffffff, v92
	v_add_f32_dpp v77, v77, v78 quad_perm:[1,0,3,2] row_mask:0xf bank_mask:0xf bound_ctrl:1
	v_cndmask_b32_e64 v78, v74, v75, s[6:7]
	v_cndmask_b32_e64 v74, v75, v74, s[6:7]
	v_cndmask_b32_e64 v75, v76, v77, s[6:7]
	v_cndmask_b32_e64 v76, v77, v76, s[6:7]
	v_add_f32_dpp v74, v78, v74 quad_perm:[2,3,0,1] row_mask:0xf bank_mask:0xf bound_ctrl:1
	v_max_f32_e32 v92, 0, v92
	v_add_f32_dpp v75, v75, v76 quad_perm:[2,3,0,1] row_mask:0xf bank_mask:0xf bound_ctrl:1
	v_cndmask_b32_e64 v76, v74, v75, s[8:9]
	v_cndmask_b32_e64 v74, v75, v74, s[8:9]
	v_mov_b32_e32 v75, v76
	v_max_f32_e32 v93, 0, v93
	s_waitcnt lgkmcnt(14)
	v_dot2c_f32_f16_e32 v104, v38, v38
	v_mov_b32_dpp v75, v75 row_shl:4 row_mask:0xf bank_mask:0x5
	v_mov_b32_e32 v105, 0
	v_dot2c_f32_f16_e32 v104, v39, v39
	v_mov_b32_dpp v75, v76 row_shr:4 row_mask:0xf bank_mask:0xa
	v_add_f32_e32 v74, v74, v75
	v_dot2c_f32_f16_e32 v104, v40, v40
	v_dot2c_f32_f16_e32 v104, v41, v41
	v_add_f32_dpp v74, v74, v74 row_ror:8 row_mask:0xf bank_mask:0xf bound_ctrl:1
	v_mov_b32_e32 v75, v74
	s_nop 1
	v_permlane16_swap_b32_e32 v74, v75
	v_add_f32_e32 v74, v74, v75
	v_mov_b32_e32 v75, v74
	s_nop 1
	v_permlane32_swap_b32_e32 v74, v75
	v_add_f32_e32 v74, v74, v75
	v_mul_f32_e32 v74, 0x3b800000, v74
	s_waitcnt lgkmcnt(13)
	v_dot2c_f32_f16_e32 v104, v34, v34
	v_readlane_b32 s42, v74, 0
	v_readlane_b32 s44, v74, 1
	v_readlane_b32 s46, v74, 2
	v_pk_add_f32 v[102:103], v[204:205], s[42:43] op_sel_hi:[1, 0] neg_lo:[0, 1] neg_hi:[0, 1]
	v_pk_add_f32 v[78:79], v[208:209], s[44:45] op_sel_hi:[1, 0] neg_lo:[0, 1] neg_hi:[0, 1]
	v_pk_add_f32 v[100:101], v[202:203], s[42:43] op_sel_hi:[1, 0] neg_lo:[0, 1] neg_hi:[0, 1]
	v_mul_f32_e32 v70, v103, v103
	v_mul_f32_e32 v71, v79, v79
	v_fmac_f32_e32 v70, v102, v102
	v_pk_add_f32 v[86:87], v[206:207], s[44:45] op_sel_hi:[1, 0] neg_lo:[0, 1] neg_hi:[0, 1]
	v_fmac_f32_e32 v71, v78, v78
	v_fmac_f32_e32 v70, v101, v101
	v_fmac_f32_e32 v71, v87, v87
	v_fmac_f32_e32 v70, v100, v100
	v_fmac_f32_e32 v71, v86, v86
	v_readlane_b32 s48, v74, 3
	v_cndmask_b32_e64 v72, v71, v70, s[4:5]
	v_cndmask_b32_e64 v70, v70, v71, s[4:5]
	v_readlane_b32 s50, v74, 4
	v_readlane_b32 s52, v74, 5
	v_readlane_b32 s54, v74, 6
	v_readlane_b32 s0, v74, 7
	v_add_f32_dpp v88, v72, v70 quad_perm:[1,0,3,2] row_mask:0xf bank_mask:0xf bound_ctrl:1
	v_pk_add_f32 v[74:75], v[212:213], s[46:47] op_sel_hi:[1, 0] neg_lo:[0, 1] neg_hi:[0, 1]
	v_pk_add_f32 v[70:71], v[216:217], s[48:49] op_sel_hi:[1, 0] neg_lo:[0, 1] neg_hi:[0, 1]
	v_pk_add_f32 v[76:77], v[210:211], s[46:47] op_sel_hi:[1, 0] neg_lo:[0, 1] neg_hi:[0, 1]
	v_mul_f32_e32 v82, v75, v75
	v_pk_add_f32 v[72:73], v[214:215], s[48:49] op_sel_hi:[1, 0] neg_lo:[0, 1] neg_hi:[0, 1]
	v_mul_f32_e32 v66, v71, v71
	v_fmac_f32_e32 v82, v74, v74
	v_fmac_f32_e32 v66, v70, v70
	v_fmac_f32_e32 v82, v77, v77
	v_fmac_f32_e32 v66, v73, v73
	v_fmac_f32_e32 v82, v76, v76
	v_fmac_f32_e32 v66, v72, v72
	v_cndmask_b32_e64 v67, v66, v82, s[4:5]
	v_cndmask_b32_e64 v66, v82, v66, s[4:5]
	v_pk_add_f32 v[68:69], v[218:219], s[50:51] op_sel_hi:[1, 0] neg_lo:[0, 1] neg_hi:[0, 1]
	v_pk_add_f32 v[62:63], v[222:223], s[52:53] op_sel_hi:[1, 0] neg_lo:[0, 1] neg_hi:[0, 1]
	v_add_f32_dpp v66, v67, v66 quad_perm:[1,0,3,2] row_mask:0xf bank_mask:0xf bound_ctrl:1
	v_cndmask_b32_e64 v67, v88, v66, s[6:7]
	v_cndmask_b32_e64 v66, v66, v88, s[6:7]
	v_pk_add_f32 v[56:57], v[228:229], s[54:55] op_sel_hi:[1, 0] neg_lo:[0, 1] neg_hi:[0, 1]
	v_dot2c_f32_f16_e32 v104, v35, v35
	v_add_f32_dpp v82, v67, v66 quad_perm:[2,3,0,1] row_mask:0xf bank_mask:0xf bound_ctrl:1
	v_pk_add_f32 v[66:67], v[220:221], s[50:51] op_sel_hi:[1, 0] neg_lo:[0, 1] neg_hi:[0, 1]
	v_pk_add_f32 v[60:61], v[224:225], s[52:53] op_sel_hi:[1, 0] neg_lo:[0, 1] neg_hi:[0, 1]
	v_mul_f32_e32 v58, v67, v67
	v_mul_f32_e32 v59, v61, v61
	v_fmac_f32_e32 v58, v66, v66
	v_fmac_f32_e32 v59, v60, v60
	v_fmac_f32_e32 v58, v69, v69
	v_fmac_f32_e32 v59, v63, v63
	v_fmac_f32_e32 v58, v68, v68
	v_fmac_f32_e32 v59, v62, v62
	v_cndmask_b32_e64 v64, v59, v58, s[4:5]
	v_cndmask_b32_e64 v58, v58, v59, s[4:5]
	v_mul_f32_e32 v65, v57, v57
	v_fmac_f32_e32 v65, v56, v56
	v_add_f32_dpp v64, v64, v58 quad_perm:[1,0,3,2] row_mask:0xf bank_mask:0xf bound_ctrl:1
	v_pk_add_f32 v[58:59], v[226:227], s[54:55] op_sel_hi:[1, 0] neg_lo:[0, 1] neg_hi:[0, 1]
	v_pk_add_f32 v[54:55], v[230:231], s[0:1] op_sel_hi:[1, 0] neg_lo:[0, 1] neg_hi:[0, 1]
	v_pk_add_f32 v[50:51], v[232:233], s[0:1] op_sel_hi:[1, 0] neg_lo:[0, 1] neg_hi:[0, 1]
	v_fmac_f32_e32 v65, v59, v59
	v_mul_f32_e32 v52, v51, v51
	v_fmac_f32_e32 v52, v50, v50
	v_fmac_f32_e32 v52, v55, v55
	v_fmac_f32_e32 v65, v58, v58
	v_fmac_f32_e32 v52, v54, v54
	v_cndmask_b32_e64 v53, v52, v65, s[4:5]
	v_cndmask_b32_e64 v52, v65, v52, s[4:5]
	v_dot2c_f32_f16_e32 v104, v36, v36
	v_dot2c_f32_f16_e32 v104, v37, v37
	v_add_f32_dpp v52, v53, v52 quad_perm:[1,0,3,2] row_mask:0xf bank_mask:0xf bound_ctrl:1
	v_cndmask_b32_e64 v53, v64, v52, s[6:7]
	v_cndmask_b32_e64 v52, v52, v64, s[6:7]
	s_waitcnt lgkmcnt(12)
	v_dot2c_f32_f16_e32 v104, v30, v30
	v_dot2c_f32_f16_e32 v104, v31, v31
	v_add_f32_dpp v52, v53, v52 quad_perm:[2,3,0,1] row_mask:0xf bank_mask:0xf bound_ctrl:1
	v_cndmask_b32_e64 v53, v82, v52, s[8:9]
	v_mov_b32_e32 v64, v53
	v_cndmask_b32_e64 v52, v52, v82, s[8:9]
	v_dot2c_f32_f16_e32 v104, v32, v32
	v_mov_b32_dpp v64, v64 row_shl:4 row_mask:0xf bank_mask:0x5
	v_dot2c_f32_f16_e32 v104, v33, v33
	s_waitcnt lgkmcnt(11)
	v_dot2c_f32_f16_e32 v104, v26, v26
	v_mov_b32_dpp v64, v53 row_shr:4 row_mask:0xf bank_mask:0xa
	v_add_f32_e32 v52, v52, v64
	v_dot2c_f32_f16_e32 v104, v27, v27
	v_dot2c_f32_f16_e32 v104, v28, v28
	v_add_f32_dpp v52, v52, v52 row_ror:8 row_mask:0xf bank_mask:0xf bound_ctrl:1
	v_mov_b32_e32 v53, v52
	s_nop 1
	v_permlane16_swap_b32_e32 v52, v53
	v_add_f32_e32 v52, v52, v53
	v_mov_b32_e32 v53, v52
	s_nop 1
	v_permlane32_swap_b32_e32 v52, v53
	v_add_f32_e32 v52, v52, v53
	v_fmac_f32_e32 v116, 0x3b800000, v52
	v_mul_f32_e32 v52, 0x4f800000, v116
	v_cmp_gt_f32_e32 vcc, s35, v116
	v_dot2c_f32_f16_e32 v104, v29, v29
	s_waitcnt lgkmcnt(10)
	v_dot2c_f32_f16_e32 v104, v22, v22
	v_cndmask_b32_e32 v64, v116, v52, vcc
	v_sqrt_f32_e32 v65, v64
	v_pk_mul_f32 v[52:53], v[94:95], v[98:99]
	v_and_b32_e32 v94, 48, v0
	v_pk_fma_f32 v[52:53], v[96:97], v[52:53], v[92:93] neg_lo:[1,0,0] neg_hi:[1,0,0]
	v_add_u32_e32 v81, -1, v65
	v_fma_f32 v82, -v81, v65, v64
	v_cmp_ge_f32_e64 s[0:1], 0, v82
	v_add_u32_e32 v82, 1, v65
	v_add_u32_e32 v95, 0x19860, v94
	v_cndmask_b32_e64 v81, v65, v81, s[0:1]
	v_fma_f32 v65, -v82, v65, v64
	v_cmp_lt_f32_e64 s[0:1], 0, v65
	v_dot2c_f32_f16_e32 v104, v23, v23
	v_dot2c_f32_f16_e32 v104, v24, v24
	v_cndmask_b32_e64 v65, v81, v82, s[0:1]
	v_mul_f32_e32 v81, 0x37800000, v65
	v_cndmask_b32_e32 v65, v65, v81, vcc
	v_cmp_class_f32_e32 vcc, v64, v117
	v_cvt_pk_f16_f32 v81, v52, v53
	ds_write_b64 v144, v[80:81] offset:36352
	v_cndmask_b32_e32 v64, v65, v64, vcc
	v_div_scale_f32 v65, s[0:1], v64, v64, 1.0
	v_rcp_f32_e32 v82, v65
	v_dot2c_f32_f16_e32 v104, v25, v25
	s_waitcnt lgkmcnt(10)
	v_dot2c_f32_f16_e32 v104, v18, v18
	v_dot2c_f32_f16_e32 v104, v19, v19
	v_fma_f32 v52, -v65, v82, 1.0
	v_fmac_f32_e32 v82, v52, v82
	v_div_scale_f32 v52, vcc, 1.0, v64, 1.0
	v_mul_f32_e32 v53, v52, v82
	v_fma_f32 v80, -v65, v53, v52
	v_fmac_f32_e32 v53, v80, v82
	v_fma_f32 v52, -v65, v53, v52
	v_div_fmas_f32 v52, v52, v82, v53
	v_div_fixup_f32 v52, v52, v64, 1.0
	v_dot2c_f32_f16_e32 v104, v20, v20
	v_readlane_b32 s0, v52, 0
	v_dot2c_f32_f16_e32 v104, v21, v21
	s_waitcnt lgkmcnt(9)
	v_dot2c_f32_f16_e32 v104, v14, v14
	v_pk_mul_f32 v[64:65], s[0:1], v[100:101] op_sel_hi:[0,1]
	v_pk_fma_f32 v[64:65], v[64:65], v[238:239], v[242:243]
	v_dot2c_f32_f16_e32 v104, v15, v15
	v_fma_f32 v53, |v64|, s25, 1.0
	v_rcp_f32_e32 v82, v53
	v_fma_f32 v53, |v65|, s25, 1.0
	v_rcp_f32_e32 v83, v53
	v_pk_mul_f32 v[84:85], v[64:65], v[64:65]
	v_and_b32_e32 v81, 0x7fffffff, v65
	v_mul_f32_e32 v53, 0xbf38aa3b, v84
	v_pk_fma_f32 v[88:89], v[82:83], s[22:23], v[90:91] op_sel_hi:[1,0,0]
	v_exp_f32_e32 v84, v53
	v_pk_fma_f32 v[88:89], v[82:83], v[88:89], s[24:25] op_sel_hi:[1,1,0]
	v_mul_f32_e32 v53, 0xbf38aa3b, v85
	v_pk_fma_f32 v[88:89], v[82:83], v[88:89], s[34:35] op_sel_hi:[1,1,0]
	v_exp_f32_e32 v85, v53
	v_pk_fma_f32 v[88:89], v[82:83], v[88:89], s[40:41] op_sel_hi:[1,1,0]
	v_and_b32_e32 v80, 0x7fffffff, v64
	v_pk_mul_f32 v[82:83], v[82:83], v[88:89]
	v_max_f32_e32 v64, 0, v64
	v_max_f32_e32 v65, 0, v65
	v_pk_mul_f32 v[80:81], v[80:81], v[82:83]
	v_dot2c_f32_f16_e32 v104, v16, v16
	v_pk_fma_f32 v[64:65], v[84:85], v[80:81], v[64:65] neg_lo:[1,0,0] neg_hi:[1,0,0]
	v_pk_mul_f32 v[80:81], s[0:1], v[102:103] op_sel_hi:[0,1]
	v_pk_fma_f32 v[80:81], v[80:81], v[240:241], v[244:245]
	v_cvt_pk_f16_f32 v64, v64, v65
	v_fma_f32 v53, |v80|, s25, 1.0
	v_rcp_f32_e32 v84, v53
	v_fma_f32 v53, |v81|, s25, 1.0
	v_rcp_f32_e32 v85, v53
	v_pk_mul_f32 v[88:89], v[80:81], v[80:81]
	v_and_b32_e32 v83, 0x7fffffff, v81
	v_mul_f32_e32 v53, 0xbf38aa3b, v88
	v_pk_fma_f32 v[92:93], v[84:85], s[22:23], v[90:91] op_sel_hi:[1,0,0]
	v_exp_f32_e32 v88, v53
	v_pk_fma_f32 v[92:93], v[84:85], v[92:93], s[24:25] op_sel_hi:[1,1,0]
	v_mul_f32_e32 v53, 0xbf38aa3b, v89
	v_pk_fma_f32 v[92:93], v[84:85], v[92:93], s[34:35] op_sel_hi:[1,1,0]
	v_exp_f32_e32 v89, v53
	v_pk_fma_f32 v[92:93], v[84:85], v[92:93], s[40:41] op_sel_hi:[1,1,0]
	v_and_b32_e32 v82, 0x7fffffff, v80
	v_pk_mul_f32 v[84:85], v[84:85], v[92:93]
	v_max_f32_e32 v80, 0, v80
	v_max_f32_e32 v81, 0, v81
	v_pk_mul_f32 v[82:83], v[82:83], v[84:85]
	v_readlane_b32 s0, v52, 1
	v_pk_fma_f32 v[80:81], v[88:89], v[82:83], v[80:81] neg_lo:[1,0,0] neg_hi:[1,0,0]
	v_dot2c_f32_f16_e32 v104, v17, v17
	v_cvt_pk_f16_f32 v65, v80, v81
	ds_write_b64 v145, v[64:65] offset:36864
	v_pk_mul_f32 v[64:65], s[0:1], v[86:87] op_sel_hi:[0,1]
	v_pk_fma_f32 v[64:65], v[64:65], v[238:239], v[242:243]
	v_pk_mul_f32 v[78:79], s[0:1], v[78:79] op_sel_hi:[0,1]
	v_fma_f32 v53, |v64|, s25, 1.0
	v_rcp_f32_e32 v82, v53
	v_fma_f32 v53, |v65|, s25, 1.0
	v_rcp_f32_e32 v83, v53
	v_pk_mul_f32 v[84:85], v[64:65], v[64:65]
	v_pk_fma_f32 v[78:79], v[78:79], v[240:241], v[244:245]
	v_mul_f32_e32 v53, 0xbf38aa3b, v84
	v_pk_fma_f32 v[86:87], v[82:83], s[22:23], v[90:91] op_sel_hi:[1,0,0]
	v_exp_f32_e32 v84, v53
	v_pk_fma_f32 v[86:87], v[82:83], v[86:87], s[24:25] op_sel_hi:[1,1,0]
	v_mul_f32_e32 v53, 0xbf38aa3b, v85
	v_pk_fma_f32 v[86:87], v[82:83], v[86:87], s[34:35] op_sel_hi:[1,1,0]
	v_and_b32_e32 v81, 0x7fffffff, v65
	v_pk_fma_f32 v[86:87], v[82:83], v[86:87], s[40:41] op_sel_hi:[1,1,0]
	v_and_b32_e32 v80, 0x7fffffff, v64
	v_exp_f32_e32 v85, v53
	v_pk_mul_f32 v[82:83], v[82:83], v[86:87]
	v_fma_f32 v53, |v78|, s25, 1.0
	v_pk_mul_f32 v[80:81], v[80:81], v[82:83]
	v_rcp_f32_e32 v82, v53
	v_fma_f32 v53, |v79|, s25, 1.0
	v_rcp_f32_e32 v83, v53
	v_max_f32_e32 v64, 0, v64
	v_max_f32_e32 v65, 0, v65
	v_pk_fma_f32 v[64:65], v[84:85], v[80:81], v[64:65] neg_lo:[1,0,0] neg_hi:[1,0,0]
	v_pk_mul_f32 v[84:85], v[78:79], v[78:79]
	v_pk_fma_f32 v[86:87], v[82:83], s[22:23], v[90:91] op_sel_hi:[1,0,0]
	v_mul_f32_e32 v53, 0xbf38aa3b, v84
	v_exp_f32_e32 v84, v53
	v_pk_fma_f32 v[86:87], v[82:83], v[86:87], s[24:25] op_sel_hi:[1,1,0]
	v_mul_f32_e32 v53, 0xbf38aa3b, v85
	v_pk_fma_f32 v[86:87], v[82:83], v[86:87], s[34:35] op_sel_hi:[1,1,0]
	v_exp_f32_e32 v85, v53
	v_pk_fma_f32 v[86:87], v[82:83], v[86:87], s[40:41] op_sel_hi:[1,1,0]
	v_and_b32_e32 v81, 0x7fffffff, v79
	v_and_b32_e32 v80, 0x7fffffff, v78
	v_pk_mul_f32 v[82:83], v[82:83], v[86:87]
	v_max_f32_e32 v78, 0, v78
	v_max_f32_e32 v79, 0, v79
	v_pk_mul_f32 v[80:81], v[80:81], v[82:83]
	v_cvt_pk_f16_f32 v64, v64, v65
	v_pk_fma_f32 v[78:79], v[84:85], v[80:81], v[78:79] neg_lo:[1,0,0] neg_hi:[1,0,0]
	v_readlane_b32 s0, v52, 2
	v_cvt_pk_f16_f32 v65, v78, v79
	ds_write_b64 v139, v[64:65] offset:37376
	v_pk_mul_f32 v[64:65], s[0:1], v[76:77] op_sel_hi:[0,1]
	v_pk_fma_f32 v[64:65], v[64:65], v[238:239], v[242:243]
	v_pk_mul_f32 v[74:75], s[0:1], v[74:75] op_sel_hi:[0,1]
	v_fma_f32 v53, |v64|, s25, 1.0
	v_rcp_f32_e32 v78, v53
	v_fma_f32 v53, |v65|, s25, 1.0
	v_rcp_f32_e32 v79, v53
	v_pk_mul_f32 v[80:81], v[64:65], v[64:65]
	v_pk_fma_f32 v[74:75], v[74:75], v[240:241], v[244:245]
	v_mul_f32_e32 v53, 0xbf38aa3b, v80
	v_pk_fma_f32 v[82:83], v[78:79], s[22:23], v[90:91] op_sel_hi:[1,0,0]
	v_exp_f32_e32 v80, v53
	v_pk_fma_f32 v[82:83], v[78:79], v[82:83], s[24:25] op_sel_hi:[1,1,0]
	v_mul_f32_e32 v53, 0xbf38aa3b, v81
	v_pk_fma_f32 v[82:83], v[78:79], v[82:83], s[34:35] op_sel_hi:[1,1,0]
	v_and_b32_e32 v77, 0x7fffffff, v65
	v_pk_fma_f32 v[82:83], v[78:79], v[82:83], s[40:41] op_sel_hi:[1,1,0]
	v_and_b32_e32 v76, 0x7fffffff, v64
	v_exp_f32_e32 v81, v53
	v_pk_mul_f32 v[78:79], v[78:79], v[82:83]
	v_fma_f32 v53, |v74|, s25, 1.0
	v_pk_mul_f32 v[76:77], v[76:77], v[78:79]
	v_rcp_f32_e32 v78, v53
	v_fma_f32 v53, |v75|, s25, 1.0
	v_rcp_f32_e32 v79, v53
	v_max_f32_e32 v64, 0, v64
	v_max_f32_e32 v65, 0, v65
	v_pk_fma_f32 v[64:65], v[80:81], v[76:77], v[64:65] neg_lo:[1,0,0] neg_hi:[1,0,0]
	v_pk_mul_f32 v[80:81], v[74:75], v[74:75]
	v_pk_fma_f32 v[82:83], v[78:79], s[22:23], v[90:91] op_sel_hi:[1,0,0]
	v_mul_f32_e32 v53, 0xbf38aa3b, v80
	v_exp_f32_e32 v80, v53
	v_pk_fma_f32 v[82:83], v[78:79], v[82:83], s[24:25] op_sel_hi:[1,1,0]
	v_mul_f32_e32 v53, 0xbf38aa3b, v81
	v_pk_fma_f32 v[82:83], v[78:79], v[82:83], s[34:35] op_sel_hi:[1,1,0]
	v_exp_f32_e32 v81, v53
	v_pk_fma_f32 v[82:83], v[78:79], v[82:83], s[40:41] op_sel_hi:[1,1,0]
	v_and_b32_e32 v77, 0x7fffffff, v75
	v_and_b32_e32 v76, 0x7fffffff, v74
	v_pk_mul_f32 v[78:79], v[78:79], v[82:83]
	v_max_f32_e32 v74, 0, v74
	v_max_f32_e32 v75, 0, v75
	v_pk_mul_f32 v[76:77], v[76:77], v[78:79]
	v_cvt_pk_f16_f32 v64, v64, v65
	v_pk_fma_f32 v[74:75], v[80:81], v[76:77], v[74:75] neg_lo:[1,0,0] neg_hi:[1,0,0]
	v_readlane_b32 s0, v52, 3
	v_cvt_pk_f16_f32 v65, v74, v75
	ds_write_b64 v137, v[64:65] offset:37888
	v_pk_mul_f32 v[64:65], s[0:1], v[72:73] op_sel_hi:[0,1]
	v_pk_fma_f32 v[64:65], v[64:65], v[238:239], v[242:243]
	v_pk_mul_f32 v[70:71], s[0:1], v[70:71] op_sel_hi:[0,1]
	v_fma_f32 v53, |v64|, s25, 1.0
	v_rcp_f32_e32 v74, v53
	v_fma_f32 v53, |v65|, s25, 1.0
	v_rcp_f32_e32 v75, v53
	v_pk_mul_f32 v[76:77], v[64:65], v[64:65]
	v_pk_fma_f32 v[70:71], v[70:71], v[240:241], v[244:245]
	v_mul_f32_e32 v53, 0xbf38aa3b, v76
	v_pk_fma_f32 v[78:79], v[74:75], s[22:23], v[90:91] op_sel_hi:[1,0,0]
	v_exp_f32_e32 v76, v53
	v_pk_fma_f32 v[78:79], v[74:75], v[78:79], s[24:25] op_sel_hi:[1,1,0]
	v_mul_f32_e32 v53, 0xbf38aa3b, v77
	v_pk_fma_f32 v[78:79], v[74:75], v[78:79], s[34:35] op_sel_hi:[1,1,0]
	v_and_b32_e32 v73, 0x7fffffff, v65
	v_pk_fma_f32 v[78:79], v[74:75], v[78:79], s[40:41] op_sel_hi:[1,1,0]
	v_and_b32_e32 v72, 0x7fffffff, v64
	v_exp_f32_e32 v77, v53
	v_pk_mul_f32 v[74:75], v[74:75], v[78:79]
	v_fma_f32 v53, |v70|, s25, 1.0
	v_pk_mul_f32 v[72:73], v[72:73], v[74:75]
	v_rcp_f32_e32 v74, v53
	v_fma_f32 v53, |v71|, s25, 1.0
	v_rcp_f32_e32 v75, v53
	v_max_f32_e32 v64, 0, v64
	v_max_f32_e32 v65, 0, v65
	v_pk_fma_f32 v[64:65], v[76:77], v[72:73], v[64:65] neg_lo:[1,0,0] neg_hi:[1,0,0]
	v_pk_mul_f32 v[76:77], v[70:71], v[70:71]
	v_pk_fma_f32 v[78:79], v[74:75], s[22:23], v[90:91] op_sel_hi:[1,0,0]
	v_mul_f32_e32 v53, 0xbf38aa3b, v76
	v_exp_f32_e32 v76, v53
	v_pk_fma_f32 v[78:79], v[74:75], v[78:79], s[24:25] op_sel_hi:[1,1,0]
	v_mul_f32_e32 v53, 0xbf38aa3b, v77
	v_pk_fma_f32 v[78:79], v[74:75], v[78:79], s[34:35] op_sel_hi:[1,1,0]
	v_exp_f32_e32 v77, v53
	v_pk_fma_f32 v[78:79], v[74:75], v[78:79], s[40:41] op_sel_hi:[1,1,0]
	v_and_b32_e32 v73, 0x7fffffff, v71
	v_and_b32_e32 v72, 0x7fffffff, v70
	v_pk_mul_f32 v[74:75], v[74:75], v[78:79]
	v_max_f32_e32 v70, 0, v70
	v_max_f32_e32 v71, 0, v71
	v_pk_mul_f32 v[72:73], v[72:73], v[74:75]
	v_cvt_pk_f16_f32 v64, v64, v65
	v_pk_fma_f32 v[70:71], v[76:77], v[72:73], v[70:71] neg_lo:[1,0,0] neg_hi:[1,0,0]
	v_readlane_b32 s0, v52, 4
	v_cvt_pk_f16_f32 v65, v70, v71
	ds_write_b64 v136, v[64:65] offset:38400
	v_pk_mul_f32 v[64:65], s[0:1], v[68:69] op_sel_hi:[0,1]
	v_pk_fma_f32 v[64:65], v[64:65], v[238:239], v[242:243]
	v_pk_mul_f32 v[66:67], s[0:1], v[66:67] op_sel_hi:[0,1]
	v_fma_f32 v53, |v64|, s25, 1.0
	v_rcp_f32_e32 v70, v53
	v_fma_f32 v53, |v65|, s25, 1.0
	v_rcp_f32_e32 v71, v53
	v_pk_mul_f32 v[72:73], v[64:65], v[64:65]
	v_pk_fma_f32 v[66:67], v[66:67], v[240:241], v[244:245]
	v_mul_f32_e32 v53, 0xbf38aa3b, v72
	v_pk_fma_f32 v[74:75], v[70:71], s[22:23], v[90:91] op_sel_hi:[1,0,0]
	v_exp_f32_e32 v72, v53
	v_pk_fma_f32 v[74:75], v[70:71], v[74:75], s[24:25] op_sel_hi:[1,1,0]
	v_mul_f32_e32 v53, 0xbf38aa3b, v73
	v_pk_fma_f32 v[74:75], v[70:71], v[74:75], s[34:35] op_sel_hi:[1,1,0]
	v_and_b32_e32 v69, 0x7fffffff, v65
	v_pk_fma_f32 v[74:75], v[70:71], v[74:75], s[40:41] op_sel_hi:[1,1,0]
	v_and_b32_e32 v68, 0x7fffffff, v64
	v_exp_f32_e32 v73, v53
	v_pk_mul_f32 v[70:71], v[70:71], v[74:75]
	v_fma_f32 v53, |v66|, s25, 1.0
	v_pk_mul_f32 v[68:69], v[68:69], v[70:71]
	v_rcp_f32_e32 v70, v53
	v_fma_f32 v53, |v67|, s25, 1.0
	v_rcp_f32_e32 v71, v53
	v_max_f32_e32 v64, 0, v64
	v_max_f32_e32 v65, 0, v65
	v_pk_fma_f32 v[64:65], v[72:73], v[68:69], v[64:65] neg_lo:[1,0,0] neg_hi:[1,0,0]
	v_pk_mul_f32 v[72:73], v[66:67], v[66:67]
	v_pk_fma_f32 v[74:75], v[70:71], s[22:23], v[90:91] op_sel_hi:[1,0,0]
	v_mul_f32_e32 v53, 0xbf38aa3b, v72
	v_exp_f32_e32 v72, v53
	v_pk_fma_f32 v[74:75], v[70:71], v[74:75], s[24:25] op_sel_hi:[1,1,0]
	v_mul_f32_e32 v53, 0xbf38aa3b, v73
	v_pk_fma_f32 v[74:75], v[70:71], v[74:75], s[34:35] op_sel_hi:[1,1,0]
	v_exp_f32_e32 v73, v53
	v_pk_fma_f32 v[74:75], v[70:71], v[74:75], s[40:41] op_sel_hi:[1,1,0]
	v_readlane_b32 s0, v52, 5
	v_and_b32_e32 v69, 0x7fffffff, v67
	v_and_b32_e32 v68, 0x7fffffff, v66
	v_pk_mul_f32 v[70:71], v[70:71], v[74:75]
	v_pk_mul_f32 v[62:63], s[0:1], v[62:63] op_sel_hi:[0,1]
	v_max_f32_e32 v66, 0, v66
	v_max_f32_e32 v67, 0, v67
	v_pk_mul_f32 v[68:69], v[68:69], v[70:71]
	v_pk_fma_f32 v[62:63], v[62:63], v[238:239], v[242:243]
	v_pk_fma_f32 v[66:67], v[72:73], v[68:69], v[66:67] neg_lo:[1,0,0] neg_hi:[1,0,0]
	v_fma_f32 v53, |v62|, s25, 1.0
	v_cvt_pk_f16_f32 v64, v64, v65
	v_cvt_pk_f16_f32 v65, v66, v67
	v_rcp_f32_e32 v66, v53
	v_fma_f32 v53, |v63|, s25, 1.0
	v_rcp_f32_e32 v67, v53
	v_pk_mul_f32 v[68:69], v[62:63], v[62:63]
	v_pk_mul_f32 v[60:61], s[0:1], v[60:61] op_sel_hi:[0,1]
	v_mul_f32_e32 v53, 0xbf38aa3b, v68
	v_pk_fma_f32 v[70:71], v[66:67], s[22:23], v[90:91] op_sel_hi:[1,0,0]
	v_exp_f32_e32 v68, v53
	v_pk_fma_f32 v[70:71], v[66:67], v[70:71], s[24:25] op_sel_hi:[1,1,0]
	v_mul_f32_e32 v53, 0xbf38aa3b, v69
	v_pk_fma_f32 v[70:71], v[66:67], v[70:71], s[34:35] op_sel_hi:[1,1,0]
	v_pk_fma_f32 v[60:61], v[60:61], v[240:241], v[244:245]
	v_pk_fma_f32 v[70:71], v[66:67], v[70:71], s[40:41] op_sel_hi:[1,1,0]
	ds_write_b64 v123, v[64:65] offset:38912
	v_and_b32_e32 v65, 0x7fffffff, v63
	v_and_b32_e32 v64, 0x7fffffff, v62
	v_exp_f32_e32 v69, v53
	v_pk_mul_f32 v[66:67], v[66:67], v[70:71]
	v_fma_f32 v53, |v60|, s25, 1.0
	v_pk_mul_f32 v[64:65], v[64:65], v[66:67]
	v_rcp_f32_e32 v66, v53
	v_fma_f32 v53, |v61|, s25, 1.0
	v_rcp_f32_e32 v67, v53
	v_max_f32_e32 v62, 0, v62
	v_max_f32_e32 v63, 0, v63
	v_pk_fma_f32 v[62:63], v[68:69], v[64:65], v[62:63] neg_lo:[1,0,0] neg_hi:[1,0,0]
	v_pk_mul_f32 v[68:69], v[60:61], v[60:61]
	v_pk_fma_f32 v[70:71], v[66:67], s[22:23], v[90:91] op_sel_hi:[1,0,0]
	v_mul_f32_e32 v53, 0xbf38aa3b, v68
	v_exp_f32_e32 v68, v53
	v_pk_fma_f32 v[70:71], v[66:67], v[70:71], s[24:25] op_sel_hi:[1,1,0]
	v_mul_f32_e32 v53, 0xbf38aa3b, v69
	v_pk_fma_f32 v[70:71], v[66:67], v[70:71], s[34:35] op_sel_hi:[1,1,0]
	v_exp_f32_e32 v69, v53
	v_pk_fma_f32 v[70:71], v[66:67], v[70:71], s[40:41] op_sel_hi:[1,1,0]
	v_and_b32_e32 v65, 0x7fffffff, v61
	v_and_b32_e32 v64, 0x7fffffff, v60
	v_pk_mul_f32 v[66:67], v[66:67], v[70:71]
	v_readlane_b32 s0, v52, 6
	v_max_f32_e32 v60, 0, v60
	v_max_f32_e32 v61, 0, v61
	v_pk_mul_f32 v[64:65], v[64:65], v[66:67]
	v_pk_mul_f32 v[58:59], s[0:1], v[58:59] op_sel_hi:[0,1]
	v_pk_fma_f32 v[60:61], v[68:69], v[64:65], v[60:61] neg_lo:[1,0,0] neg_hi:[1,0,0]
	v_pk_fma_f32 v[58:59], v[58:59], v[238:239], v[242:243]
	v_cvt_pk_f16_f32 v62, v62, v63
	v_cvt_pk_f16_f32 v63, v60, v61
	v_fma_f32 v53, |v58|, s25, 1.0
	ds_write_b64 v133, v[62:63] offset:39424
	v_rcp_f32_e32 v62, v53
	v_fma_f32 v53, |v59|, s25, 1.0
	v_rcp_f32_e32 v63, v53
	v_pk_mul_f32 v[64:65], v[58:59], v[58:59]
	v_pk_mul_f32 v[56:57], s[0:1], v[56:57] op_sel_hi:[0,1]
	v_mul_f32_e32 v53, 0xbf38aa3b, v64
	v_pk_fma_f32 v[66:67], v[62:63], s[22:23], v[90:91] op_sel_hi:[1,0,0]
	v_exp_f32_e32 v64, v53
	v_pk_fma_f32 v[66:67], v[62:63], v[66:67], s[24:25] op_sel_hi:[1,1,0]
	v_mul_f32_e32 v53, 0xbf38aa3b, v65
	v_pk_fma_f32 v[66:67], v[62:63], v[66:67], s[34:35] op_sel_hi:[1,1,0]
	v_exp_f32_e32 v65, v53
	v_pk_fma_f32 v[66:67], v[62:63], v[66:67], s[40:41] op_sel_hi:[1,1,0]
	v_pk_fma_f32 v[56:57], v[56:57], v[240:241], v[244:245]
	v_and_b32_e32 v61, 0x7fffffff, v59
	v_and_b32_e32 v60, 0x7fffffff, v58
	v_pk_mul_f32 v[62:63], v[62:63], v[66:67]
	v_fma_f32 v53, |v56|, s25, 1.0
	v_pk_mul_f32 v[60:61], v[60:61], v[62:63]
	v_rcp_f32_e32 v62, v53
	v_fma_f32 v53, |v57|, s25, 1.0
	v_max_f32_e32 v58, 0, v58
	v_max_f32_e32 v59, 0, v59
	v_rcp_f32_e32 v63, v53
	v_pk_fma_f32 v[58:59], v[64:65], v[60:61], v[58:59] neg_lo:[1,0,0] neg_hi:[1,0,0]
	v_pk_mul_f32 v[64:65], v[56:57], v[56:57]
	v_readlane_b32 s0, v52, 7
	v_mul_f32_e32 v53, 0xbf38aa3b, v64
	v_exp_f32_e32 v64, v53
	v_mul_f32_e32 v53, 0xbf38aa3b, v65
	v_pk_fma_f32 v[66:67], v[62:63], s[22:23], v[90:91] op_sel_hi:[1,0,0]
	v_exp_f32_e32 v65, v53
	v_pk_mul_f32 v[52:53], s[0:1], v[54:55] op_sel_hi:[0,1]
	v_pk_fma_f32 v[66:67], v[62:63], v[66:67], s[24:25] op_sel_hi:[1,1,0]
	v_pk_fma_f32 v[42:43], v[52:53], v[238:239], v[242:243]
	v_pk_fma_f32 v[66:67], v[62:63], v[66:67], s[34:35] op_sel_hi:[1,1,0]
	v_fma_f32 v52, |v42|, s25, 1.0
	v_fma_f32 v53, |v43|, s25, 1.0
	v_pk_fma_f32 v[66:67], v[62:63], v[66:67], s[40:41] op_sel_hi:[1,1,0]
	v_rcp_f32_e32 v52, v52
	v_rcp_f32_e32 v53, v53
	v_and_b32_e32 v61, 0x7fffffff, v57
	v_and_b32_e32 v60, 0x7fffffff, v56
	v_pk_mul_f32 v[62:63], v[62:63], v[66:67]
	v_max_f32_e32 v56, 0, v56
	v_max_f32_e32 v57, 0, v57
	v_pk_mul_f32 v[60:61], v[60:61], v[62:63]
	v_cvt_pk_f16_f32 v58, v58, v59
	v_pk_fma_f32 v[56:57], v[64:65], v[60:61], v[56:57] neg_lo:[1,0,0] neg_hi:[1,0,0]
	v_pk_mul_f32 v[54:55], v[42:43], v[42:43]
	v_cvt_pk_f16_f32 v59, v56, v57
	v_pk_fma_f32 v[56:57], v[52:53], s[22:23], v[90:91] op_sel_hi:[1,0,0]
	v_mul_f32_e32 v54, 0xbf38aa3b, v54
	v_pk_fma_f32 v[56:57], v[52:53], v[56:57], s[24:25] op_sel_hi:[1,1,0]
	v_mul_f32_e32 v55, 0xbf38aa3b, v55
	v_exp_f32_e32 v54, v54
	v_pk_fma_f32 v[56:57], v[52:53], v[56:57], s[34:35] op_sel_hi:[1,1,0]
	v_exp_f32_e32 v55, v55
	v_pk_fma_f32 v[56:57], v[52:53], v[56:57], s[40:41] op_sel_hi:[1,1,0]
	v_and_b32_e32 v47, 0x7fffffff, v43
	v_and_b32_e32 v46, 0x7fffffff, v42
	v_pk_mul_f32 v[52:53], v[52:53], v[56:57]
	v_max_f32_e32 v42, 0, v42
	v_max_f32_e32 v43, 0, v43
	v_pk_mul_f32 v[46:47], v[46:47], v[52:53]
	ds_write_b64 v119, v[58:59] offset:39936
	v_pk_fma_f32 v[42:43], v[54:55], v[46:47], v[42:43] neg_lo:[1,0,0] neg_hi:[1,0,0]
	v_pk_mul_f32 v[46:47], s[0:1], v[50:51] op_sel_hi:[0,1]
	v_pk_fma_f32 v[44:45], v[46:47], v[240:241], v[244:245]
	v_cvt_pk_f16_f32 v42, v42, v43
	v_fma_f32 v43, |v44|, s25, 1.0
	v_rcp_f32_e32 v48, v43
	v_fma_f32 v43, |v45|, s25, 1.0
	v_rcp_f32_e32 v49, v43
	v_pk_mul_f32 v[50:51], v[44:45], v[44:45]
	v_and_b32_e32 v47, 0x7fffffff, v45
	v_mul_f32_e32 v43, 0xbf38aa3b, v50
	v_pk_fma_f32 v[52:53], v[48:49], s[22:23], v[90:91] op_sel_hi:[1,0,0]
	v_exp_f32_e32 v50, v43
	v_pk_fma_f32 v[52:53], v[48:49], v[52:53], s[24:25] op_sel_hi:[1,1,0]
	v_mul_f32_e32 v43, 0xbf38aa3b, v51
	v_pk_fma_f32 v[52:53], v[48:49], v[52:53], s[34:35] op_sel_hi:[1,1,0]
	v_exp_f32_e32 v51, v43
	v_pk_fma_f32 v[52:53], v[48:49], v[52:53], s[40:41] op_sel_hi:[1,1,0]
	v_and_b32_e32 v46, 0x7fffffff, v44
	v_pk_mul_f32 v[48:49], v[48:49], v[52:53]
	v_max_f32_e32 v44, 0, v44
	v_max_f32_e32 v45, 0, v45
	v_pk_mul_f32 v[46:47], v[46:47], v[48:49]
	s_waitcnt lgkmcnt(14)
	v_dot2c_f32_f16_e32 v104, v10, v10
	v_pk_fma_f32 v[44:45], v[50:51], v[46:47], v[44:45] neg_lo:[1,0,0] neg_hi:[1,0,0]
	v_dot2c_f32_f16_e32 v104, v11, v11
	v_cvt_pk_f16_f32 v43, v44, v45
	ds_write_b64 v146, v[42:43] offset:40448
	ds_read_b128 v[70:73], v115 offset:32768
	ds_read_b128 v[66:69], v147 offset:32768
	ds_read_b128 v[62:65], v148 offset:32768
	ds_read_b128 v[58:61], v149 offset:32768
	ds_read_b128 v[54:57], v150 offset:33024
	ds_read_b128 v[50:53], v151 offset:33024
	ds_read_b128 v[46:49], v152 offset:33024
	ds_read_b128 v[42:45], v153 offset:33024
	ds_read_b128 v[74:77], v95
	ds_read_b128 v[78:81], v95 offset:64
	ds_read_b128 v[82:85], v95 offset:128
	ds_read_b128 v[86:89], v95 offset:192
	ds_read_b128 v[90:93], v95 offset:256
	ds_read_b128 v[96:99], v95 offset:320
	s_waitcnt lgkmcnt(5)
	v_dot2c_f32_f16_e32 v105, v38, v74
	v_dot2c_f32_f16_e32 v105, v39, v75
	ds_read_b128 v[100:103], v95 offset:384
	ds_read_b128 v[108:111], v95 offset:448
	v_mov_b32_e32 v95, 0
	v_dot2c_f32_f16_e32 v105, v40, v76
	v_dot2c_f32_f16_e32 v95, v70, v70
	v_dot2c_f32_f16_e32 v105, v41, v77
	v_mov_b32_e32 v115, 0
	v_dot2c_f32_f16_e32 v95, v71, v71
	s_waitcnt lgkmcnt(6)
	v_dot2c_f32_f16_e32 v105, v34, v78
	v_dot2c_f32_f16_e32 v115, v70, v74
	v_dot2c_f32_f16_e32 v95, v72, v72
	v_dot2c_f32_f16_e32 v105, v35, v79
	v_dot2c_f32_f16_e32 v115, v71, v75
	v_dot2c_f32_f16_e32 v95, v73, v73
	v_dot2c_f32_f16_e32 v105, v36, v80
	v_dot2c_f32_f16_e32 v115, v72, v76
	v_dot2c_f32_f16_e32 v95, v66, v66
	v_dot2c_f32_f16_e32 v105, v37, v81
	v_dot2c_f32_f16_e32 v115, v73, v77
	v_dot2c_f32_f16_e32 v95, v67, v67
	s_waitcnt lgkmcnt(5)
	v_dot2c_f32_f16_e32 v105, v30, v82
	v_dot2c_f32_f16_e32 v115, v66, v78
	v_dot2c_f32_f16_e32 v95, v68, v68
	v_dot2c_f32_f16_e32 v105, v31, v83
	v_dot2c_f32_f16_e32 v115, v67, v79
	v_dot2c_f32_f16_e32 v95, v69, v69
	v_dot2c_f32_f16_e32 v105, v32, v84
	v_dot2c_f32_f16_e32 v115, v68, v80
	v_dot2c_f32_f16_e32 v95, v62, v62
	v_dot2c_f32_f16_e32 v105, v33, v85
	v_dot2c_f32_f16_e32 v115, v69, v81
	v_dot2c_f32_f16_e32 v95, v63, v63
	s_waitcnt lgkmcnt(4)
	v_dot2c_f32_f16_e32 v105, v26, v86
	v_dot2c_f32_f16_e32 v115, v62, v82
	v_dot2c_f32_f16_e32 v95, v64, v64
	v_dot2c_f32_f16_e32 v105, v27, v87
	v_dot2c_f32_f16_e32 v115, v63, v83
	v_dot2c_f32_f16_e32 v95, v65, v65
	v_dot2c_f32_f16_e32 v105, v28, v88
	v_dot2c_f32_f16_e32 v115, v64, v84
	v_dot2c_f32_f16_e32 v95, v58, v58
	v_dot2c_f32_f16_e32 v105, v29, v89
	v_dot2c_f32_f16_e32 v115, v65, v85
	v_dot2c_f32_f16_e32 v95, v59, v59
	s_waitcnt lgkmcnt(3)
	v_dot2c_f32_f16_e32 v105, v22, v90
	v_dot2c_f32_f16_e32 v115, v58, v86
	v_dot2c_f32_f16_e32 v95, v60, v60
	v_dot2c_f32_f16_e32 v105, v23, v91
	v_dot2c_f32_f16_e32 v115, v59, v87
	v_dot2c_f32_f16_e32 v95, v61, v61
	v_dot2c_f32_f16_e32 v105, v24, v92
	v_dot2c_f32_f16_e32 v115, v60, v88
	v_dot2c_f32_f16_e32 v95, v54, v54
	v_dot2c_f32_f16_e32 v105, v25, v93
	v_dot2c_f32_f16_e32 v115, v61, v89
	v_dot2c_f32_f16_e32 v95, v55, v55
	s_waitcnt lgkmcnt(2)
	v_dot2c_f32_f16_e32 v105, v18, v96
	v_dot2c_f32_f16_e32 v115, v54, v90
	v_dot2c_f32_f16_e32 v95, v56, v56
	v_dot2c_f32_f16_e32 v105, v19, v97
	v_dot2c_f32_f16_e32 v115, v55, v91
	v_dot2c_f32_f16_e32 v95, v57, v57
	v_dot2c_f32_f16_e32 v105, v20, v98
	v_dot2c_f32_f16_e32 v115, v56, v92
	v_dot2c_f32_f16_e32 v95, v50, v50
	v_dot2c_f32_f16_e32 v105, v21, v99
	v_dot2c_f32_f16_e32 v115, v57, v93
	v_dot2c_f32_f16_e32 v95, v51, v51
	s_waitcnt lgkmcnt(1)
	v_dot2c_f32_f16_e32 v105, v14, v100
	v_dot2c_f32_f16_e32 v115, v50, v96
	v_dot2c_f32_f16_e32 v95, v52, v52
	v_dot2c_f32_f16_e32 v105, v15, v101
	v_dot2c_f32_f16_e32 v115, v51, v97
	v_dot2c_f32_f16_e32 v95, v53, v53
	v_dot2c_f32_f16_e32 v105, v16, v102
	v_dot2c_f32_f16_e32 v115, v52, v98
	v_dot2c_f32_f16_e32 v95, v46, v46
	v_dot2c_f32_f16_e32 v105, v17, v103
	v_dot2c_f32_f16_e32 v115, v53, v99
	v_dot2c_f32_f16_e32 v95, v47, v47
	s_waitcnt lgkmcnt(0)
	v_dot2c_f32_f16_e32 v105, v10, v108
	v_dot2c_f32_f16_e32 v104, v12, v12
	v_dot2c_f32_f16_e32 v115, v46, v100
	v_dot2c_f32_f16_e32 v95, v48, v48
	v_dot2c_f32_f16_e32 v105, v11, v109
	v_dot2c_f32_f16_e32 v104, v13, v13
	v_dot2c_f32_f16_e32 v115, v47, v101
	v_dot2c_f32_f16_e32 v95, v49, v49
	v_dot2c_f32_f16_e32 v105, v12, v110
	v_dot2c_f32_f16_e32 v115, v48, v102
	v_dot2c_f32_f16_e32 v95, v42, v42
	v_mov_b32_e32 v74, v104
	v_dot2c_f32_f16_e32 v105, v13, v111
	v_dot2c_f32_f16_e32 v115, v49, v103
	v_dot2c_f32_f16_e32 v95, v43, v43
	v_permlane16_swap_b32_e32 v104, v74
	v_dot2c_f32_f16_e32 v115, v42, v108
	v_dot2c_f32_f16_e32 v95, v44, v44
	v_add_f32_e32 v133, v104, v74
	v_mov_b32_e32 v74, v105
	v_dot2c_f32_f16_e32 v115, v43, v109
	v_dot2c_f32_f16_e32 v95, v45, v45
	v_permlane16_swap_b32_e32 v105, v74
	v_dot2c_f32_f16_e32 v115, v44, v110
	v_add_f32_e32 v137, v105, v74
	v_mov_b32_e32 v74, v95
	v_dot2c_f32_f16_e32 v115, v45, v111
	s_nop 0
	v_permlane16_swap_b32_e32 v95, v74
	v_add_f32_e32 v135, v95, v74
	v_mov_b32_e32 v74, v115
	s_nop 1
	v_permlane16_swap_b32_e32 v115, v74
	v_add_f32_e32 v139, v115, v74
	v_lshlrev_b32_e32 v74, 8, v107
	v_lshlrev_b32_e32 v75, 3, v114
	s_movk_i32 s0, 0x78
	v_and_or_b32 v76, v75, s0, v74
	v_lshlrev_b32_e32 v75, 3, v141
	v_and_or_b32 v77, v75, s0, v74
	v_lshlrev_b32_e32 v75, 3, v142
	v_and_or_b32 v78, v75, s0, v74
	v_lshlrev_b32_e32 v75, 3, v143
	v_and_or_b32 v79, v75, s0, v74
	s_add_u32 s0, s26, 0x8000
	v_or_b32_e32 v108, 0x8000, v112
	v_mov_b32_e32 v123, 0
	s_addc_u32 s1, s27, 0
	v_readfirstlane_b32 s4, v108
	s_waitcnt vmcnt(0)
	s_barrier
	v_lshl_add_u64 v[74:75], s[0:1], 0, v[122:123]
	s_mov_b32 m0, s4
	s_nop 0
	global_load_lds_dwordx4 v[74:75], off
	s_addk_i32 s4, 0x400
	v_mov_b32_e32 v107, v123
	v_lshl_add_u64 v[74:75], s[0:1], 0, v[106:107]
	s_add_u32 s0, s26, 0xc000
	s_mov_b32 m0, s4
	s_nop 0
	global_load_lds_dwordx4 v[74:75], off
	s_addc_u32 s1, s27, 0
	v_or_b32_e32 v109, 0xc000, v112
	v_lshl_add_u64 v[74:75], s[0:1], 0, v[122:123]
	v_readfirstlane_b32 s4, v109
	s_mov_b32 m0, s4
	s_nop 0
	global_load_lds_dwordx4 v[74:75], off
	s_addk_i32 s4, 0x400
	v_lshl_add_u64 v[74:75], s[0:1], 0, v[106:107]
	s_mov_b32 m0, s4
	s_nop 0
	global_load_lds_dwordx4 v[74:75], off
	v_mov_b32_e32 v134, v133
	v_mov_b32_e32 v138, v137
	v_mov_b32_e32 v136, v135
	v_mov_b32_e32 v140, v139
	v_lshlrev_b32_e32 v144, 1, v76
	v_lshlrev_b32_e32 v143, 1, v77
	v_lshlrev_b32_e32 v142, 1, v78
	v_lshlrev_b32_e32 v141, 1, v79
	s_add_u32 s0, s26, 0x14000
	v_mov_b32_e32 v74, 0x7f61b1e6
	v_permlane32_swap_b32_e32 v133, v134
	v_permlane32_swap_b32_e32 v137, v138
	v_permlane32_swap_b32_e32 v135, v136
	v_permlane32_swap_b32_e32 v139, v140
	v_or_b32_e32 v160, 0x10000, v144
	v_or_b32_e32 v158, 0x10000, v143
	v_or_b32_e32 v156, 0x10000, v142
	v_or_b32_e32 v154, 0x10000, v141
	v_or_b32_e32 v159, 0x12000, v144
	v_or_b32_e32 v157, 0x12000, v143
	v_or_b32_e32 v155, 0x12000, v142
	v_or_b32_e32 v153, 0x12000, v141
	v_or_b32_e32 v152, 0x14000, v144
	v_or_b32_e32 v150, 0x14000, v143
	v_or_b32_e32 v148, 0x14000, v142
	v_or_b32_e32 v146, 0x14000, v141
	v_or_b32_e32 v151, 0x16000, v144
	v_or_b32_e32 v149, 0x16000, v143
	v_or_b32_e32 v147, 0x16000, v142
	v_or_b32_e32 v145, 0x16000, v141
	s_addc_u32 s1, s27, 0
	v_mov_b32_e32 v98, 0x7f800000
	s_mov_b32 s22, 0
	v_mov_b32_e32 v100, 0x7f800000
	v_mov_b32_e32 v99, 0x7f800000
	v_mov_b32_e32 v111, 0x7f800000
	v_mov_b32_e32 v101, 0x7f800000
	v_mov_b32_e32 v110, 0x7f800000
	v_mov_b32_e32 v75, v74
	v_mov_b32_e32 v76, v74
	v_mov_b32_e32 v77, v74
	v_mov_b32_e32 v78, v74
	v_mov_b32_e32 v79, v74
	v_mov_b32_e32 v80, v74
	v_mov_b32_e32 v81, v74
	v_mov_b32_e32 v82, v74
	v_mov_b32_e32 v83, v74
	v_mov_b32_e32 v84, v74
	v_mov_b32_e32 v85, v74
	v_mov_b32_e32 v86, v74
	v_mov_b32_e32 v87, v74
	v_mov_b32_e32 v88, v74
	v_mov_b32_e32 v89, v74
	v_mov_b32_e32 v247, 0xfffffc00
	v_readfirstlane_b32 s96, v1
	s_nop 3
	s_cmp_lt_u32 s96, 4
	s_cbranch_scc0 .Lmy_prio_done
	s_setprio 1
